# v18 + GEMM K loops: first pass peeled with C=0 MFMAs, the 128 accumulator-zeroing moves per unit removed (all five instances)
# speedup vs baseline: 1.0043x; 1.0043x over previous
.LBB0_308:
	v_mov_b32_e32 v0, 0
	s_mov_b32 s17, -2
	s_mov_b64 s[2:3], 0
	v_mov_b32_e32 v1, v0
	s_waitcnt lgkmcnt(0)
	s_add_u32 s33, s22, s2
	s_addc_u32 s61, s23, s3
	v_add_u32_e32 v132, 0x10000, v136
	v_add_u32_e32 v138, 0x14000, v136
	s_add_u32 s34, s33, 0x100
	ds_read_b128 v[140:143], v132
	ds_read_b128 v[144:147], v132 offset:1024
	ds_read_b128 v[148:151], v132 offset:2048
	ds_read_b128 v[152:155], v132 offset:3072
	ds_read_b128 v[156:159], v138
	ds_read_b128 v[160:163], v138 offset:1024
	ds_read_b128 v[164:167], v138 offset:2048
	ds_read_b128 v[168:171], v138 offset:3072
	s_addc_u32 s35, s61, 0
	s_add_u32 s26, s33, 0x180
	s_addc_u32 s27, s61, 0
	s_add_u32 s19, s24, s2
	s_addc_u32 s21, s25, s3
	s_add_u32 s36, s19, 0x100
	s_addc_u32 s37, s21, 0
	ds_read_b128 v[172:175], v137
	ds_read_b128 v[176:179], v137 offset:1024
	ds_read_b128 v[180:183], v137 offset:2048
	ds_read_b128 v[184:187], v137 offset:3072
	ds_read_b128 v[188:191], v137 offset:4096
	ds_read_b128 v[194:197], v137 offset:5120
	ds_read_b128 v[202:205], v137 offset:6144
	ds_read_b128 v[206:209], v137 offset:7168
	s_add_u32 s62, s33, 0x40080
	s_addc_u32 s63, s61, 0
	s_mov_b32 m0, s57
	s_nop 0
	global_load_lds_dwordx4 v65, s[62:63]
	s_nop 0
	s_mov_b32 m0, s59
	s_nop 0
	global_load_lds_dwordx4 v134, s[62:63]
	s_waitcnt vmcnt(8)
	s_waitcnt lgkmcnt(0)
	s_barrier
	s_setprio 1
	s_waitcnt lgkmcnt(0)
	v_mfma_f32_16x16x32_bf16 v[128:131], v[140:143], v[172:175], 0
	v_mfma_f32_16x16x32_bf16 v[124:127], v[148:151], v[172:175], 0
	v_mfma_f32_16x16x32_bf16 v[120:123], v[140:143], v[180:183], 0
	v_mfma_f32_16x16x32_bf16 v[116:119], v[148:151], v[180:183], 0
	v_mfma_f32_16x16x32_bf16 v[110:113], v[140:143], v[188:191], 0
	v_mfma_f32_16x16x32_bf16 v[106:109], v[148:151], v[188:191], 0
	v_mfma_f32_16x16x32_bf16 v[102:105], v[140:143], v[202:205], 0
	v_mfma_f32_16x16x32_bf16 v[98:101], v[148:151], v[202:205], 0
	v_mfma_f32_16x16x32_bf16 v[128:131], v[144:147], v[176:179], v[128:131]
	v_mfma_f32_16x16x32_bf16 v[124:127], v[152:155], v[176:179], v[124:127]
	v_mfma_f32_16x16x32_bf16 v[120:123], v[144:147], v[184:187], v[120:123]
	v_mfma_f32_16x16x32_bf16 v[116:119], v[152:155], v[184:187], v[116:119]
	v_mfma_f32_16x16x32_bf16 v[110:113], v[144:147], v[194:197], v[110:113]
	v_mfma_f32_16x16x32_bf16 v[106:109], v[152:155], v[194:197], v[106:109]
	v_mfma_f32_16x16x32_bf16 v[102:105], v[144:147], v[206:209], v[102:105]
	v_mfma_f32_16x16x32_bf16 v[98:101], v[152:155], v[206:209], v[98:101]
	s_setprio 0
	s_setprio 1
	v_mfma_f32_16x16x32_bf16 v[94:97], v[156:159], v[172:175], 0
	v_mfma_f32_16x16x32_bf16 v[90:93], v[164:167], v[172:175], 0
	v_mfma_f32_16x16x32_bf16 v[86:89], v[156:159], v[180:183], 0
	v_mfma_f32_16x16x32_bf16 v[82:85], v[164:167], v[180:183], 0
	v_mfma_f32_16x16x32_bf16 v[78:81], v[156:159], v[188:191], 0
	v_mfma_f32_16x16x32_bf16 v[74:77], v[164:167], v[188:191], 0
	v_mfma_f32_16x16x32_bf16 v[70:73], v[156:159], v[202:205], 0
	v_mfma_f32_16x16x32_bf16 v[66:69], v[164:167], v[202:205], 0
	v_mfma_f32_16x16x32_bf16 v[94:97], v[160:163], v[176:179], v[94:97]
	v_mfma_f32_16x16x32_bf16 v[90:93], v[168:171], v[176:179], v[90:93]
	v_mfma_f32_16x16x32_bf16 v[86:89], v[160:163], v[184:187], v[86:89]
	v_mfma_f32_16x16x32_bf16 v[82:85], v[168:171], v[184:187], v[82:85]
	v_mfma_f32_16x16x32_bf16 v[78:81], v[160:163], v[194:197], v[78:81]
	v_mfma_f32_16x16x32_bf16 v[74:77], v[168:171], v[194:197], v[74:77]
	v_mfma_f32_16x16x32_bf16 v[70:73], v[160:163], v[206:209], v[70:73]
	v_mfma_f32_16x16x32_bf16 v[66:69], v[168:171], v[206:209], v[66:69]
	s_setprio 0
	s_barrier
	ds_read_b128 v[172:175], v137 offset:16384
	ds_read_b128 v[176:179], v137 offset:17408
	ds_read_b128 v[180:183], v137 offset:18432
	ds_read_b128 v[184:187], v137 offset:19456
	ds_read_b128 v[188:191], v137 offset:20480
	ds_read_b128 v[194:197], v137 offset:21504
	ds_read_b128 v[202:205], v137 offset:22528
	ds_read_b128 v[206:209], v137 offset:23552
	s_mov_b32 m0, s41
	s_nop 0
	global_load_lds_dwordx4 v114, s[36:37]
	s_nop 0
	s_mov_b32 m0, s42
	s_nop 0
	global_load_lds_dwordx4 v135, s[36:37]
	s_add_u32 s36, s19, 0x40100
	s_addc_u32 s37, s21, 0
	s_mov_b32 m0, s43
	s_nop 0
	global_load_lds_dwordx4 v114, s[36:37]
	s_nop 0
	s_mov_b32 m0, s44
	s_nop 0
	global_load_lds_dwordx4 v135, s[36:37]
	s_mov_b32 m0, s40
	s_nop 0
	global_load_lds_dwordx4 v65, s[34:35]
	s_nop 0
	s_mov_b32 m0, s45
	s_nop 0
	global_load_lds_dwordx4 v134, s[34:35]
	s_waitcnt vmcnt(8)
	s_waitcnt lgkmcnt(0)
	s_barrier
	s_setprio 1
	s_waitcnt lgkmcnt(0)
	v_mfma_f32_16x16x32_bf16 v[60:63], v[140:143], v[172:175], 0
	v_mfma_f32_16x16x32_bf16 v[56:59], v[148:151], v[172:175], 0
	s_waitcnt lgkmcnt(5)
	v_mfma_f32_16x16x32_bf16 v[52:55], v[140:143], v[180:183], 0
	v_mfma_f32_16x16x32_bf16 v[48:51], v[148:151], v[180:183], 0
	s_waitcnt lgkmcnt(3)
	v_mfma_f32_16x16x32_bf16 v[44:47], v[140:143], v[188:191], 0
	v_mfma_f32_16x16x32_bf16 v[40:43], v[148:151], v[188:191], 0
	s_waitcnt lgkmcnt(1)
	v_mfma_f32_16x16x32_bf16 v[36:39], v[140:143], v[202:205], 0
	v_mfma_f32_16x16x32_bf16 v[32:35], v[148:151], v[202:205], 0
	v_mfma_f32_16x16x32_bf16 v[60:63], v[144:147], v[176:179], v[60:63]
	v_mfma_f32_16x16x32_bf16 v[56:59], v[152:155], v[176:179], v[56:59]
	v_mfma_f32_16x16x32_bf16 v[52:55], v[144:147], v[184:187], v[52:55]
	v_mfma_f32_16x16x32_bf16 v[48:51], v[152:155], v[184:187], v[48:51]
	v_mfma_f32_16x16x32_bf16 v[44:47], v[144:147], v[194:197], v[44:47]
	v_mfma_f32_16x16x32_bf16 v[40:43], v[152:155], v[194:197], v[40:43]
	s_waitcnt lgkmcnt(0)
	v_mfma_f32_16x16x32_bf16 v[36:39], v[144:147], v[206:209], v[36:39]
	v_mfma_f32_16x16x32_bf16 v[32:35], v[152:155], v[206:209], v[32:35]
	s_setprio 0
	s_setprio 1
	v_mfma_f32_16x16x32_bf16 v[28:31], v[156:159], v[172:175], 0
	v_mfma_f32_16x16x32_bf16 v[24:27], v[164:167], v[172:175], 0
	v_mfma_f32_16x16x32_bf16 v[20:23], v[156:159], v[180:183], 0
	v_mfma_f32_16x16x32_bf16 v[16:19], v[164:167], v[180:183], 0
	v_mfma_f32_16x16x32_bf16 v[12:15], v[156:159], v[188:191], 0
	v_mfma_f32_16x16x32_bf16 v[8:11], v[164:167], v[188:191], 0
	v_mfma_f32_16x16x32_bf16 v[4:7], v[156:159], v[202:205], 0
	v_mfma_f32_16x16x32_bf16 v[0:3], v[164:167], v[202:205], 0
	v_mfma_f32_16x16x32_bf16 v[28:31], v[160:163], v[176:179], v[28:31]
	v_mfma_f32_16x16x32_bf16 v[24:27], v[168:171], v[176:179], v[24:27]
	v_mfma_f32_16x16x32_bf16 v[20:23], v[160:163], v[184:187], v[20:23]
	v_mfma_f32_16x16x32_bf16 v[16:19], v[168:171], v[184:187], v[16:19]
	v_mfma_f32_16x16x32_bf16 v[12:15], v[160:163], v[194:197], v[12:15]
	v_mfma_f32_16x16x32_bf16 v[8:11], v[168:171], v[194:197], v[8:11]
	v_mfma_f32_16x16x32_bf16 v[4:7], v[160:163], v[206:209], v[4:7]
	v_mfma_f32_16x16x32_bf16 v[0:3], v[168:171], v[206:209], v[0:3]
	s_setprio 0
	s_barrier
	v_add_u32_e32 v133, 0x18000, v136
	v_add_u32_e32 v139, 0x1c000, v136
	ds_read_b128 v[140:143], v133
	ds_read_b128 v[144:147], v133 offset:1024
	ds_read_b128 v[148:151], v133 offset:2048
	ds_read_b128 v[152:155], v133 offset:3072
	ds_read_b128 v[156:159], v139
	ds_read_b128 v[160:163], v139 offset:1024
	ds_read_b128 v[164:167], v139 offset:2048
	ds_read_b128 v[168:171], v139 offset:3072
	ds_read_b128 v[172:175], v137 offset:32768
	ds_read_b128 v[176:179], v137 offset:33792
	ds_read_b128 v[180:183], v137 offset:34816
	ds_read_b128 v[184:187], v137 offset:35840
	ds_read_b128 v[188:191], v137 offset:36864
	ds_read_b128 v[194:197], v137 offset:37888
	ds_read_b128 v[202:205], v137 offset:38912
	ds_read_b128 v[206:209], v137 offset:39936
	s_add_u32 s34, s33, 0x40100
	s_addc_u32 s35, s61, 0
	s_mov_b32 m0, s46
	s_nop 0
	global_load_lds_dwordx4 v65, s[34:35]
	s_nop 0
	s_mov_b32 m0, s47
	s_nop 0
	global_load_lds_dwordx4 v134, s[34:35]
	s_waitcnt vmcnt(8)
	s_waitcnt lgkmcnt(0)
	s_barrier
	s_setprio 1
	s_waitcnt lgkmcnt(0)
	v_mfma_f32_16x16x32_bf16 v[128:131], v[140:143], v[172:175], v[128:131]
	v_mfma_f32_16x16x32_bf16 v[124:127], v[148:151], v[172:175], v[124:127]
	s_waitcnt lgkmcnt(5)
	v_mfma_f32_16x16x32_bf16 v[120:123], v[140:143], v[180:183], v[120:123]
	v_mfma_f32_16x16x32_bf16 v[116:119], v[148:151], v[180:183], v[116:119]
	s_waitcnt lgkmcnt(3)
	v_mfma_f32_16x16x32_bf16 v[110:113], v[140:143], v[188:191], v[110:113]
	v_mfma_f32_16x16x32_bf16 v[106:109], v[148:151], v[188:191], v[106:109]
	s_waitcnt lgkmcnt(1)
	v_mfma_f32_16x16x32_bf16 v[102:105], v[140:143], v[202:205], v[102:105]
	v_mfma_f32_16x16x32_bf16 v[98:101], v[148:151], v[202:205], v[98:101]
	v_mfma_f32_16x16x32_bf16 v[128:131], v[144:147], v[176:179], v[128:131]
	v_mfma_f32_16x16x32_bf16 v[124:127], v[152:155], v[176:179], v[124:127]
	v_mfma_f32_16x16x32_bf16 v[120:123], v[144:147], v[184:187], v[120:123]
	v_mfma_f32_16x16x32_bf16 v[116:119], v[152:155], v[184:187], v[116:119]
	v_mfma_f32_16x16x32_bf16 v[110:113], v[144:147], v[194:197], v[110:113]
	v_mfma_f32_16x16x32_bf16 v[106:109], v[152:155], v[194:197], v[106:109]
	s_waitcnt lgkmcnt(0)
	v_mfma_f32_16x16x32_bf16 v[102:105], v[144:147], v[206:209], v[102:105]
	v_mfma_f32_16x16x32_bf16 v[98:101], v[152:155], v[206:209], v[98:101]
	s_setprio 0
	s_setprio 1
	v_mfma_f32_16x16x32_bf16 v[94:97], v[156:159], v[172:175], v[94:97]
	v_mfma_f32_16x16x32_bf16 v[90:93], v[164:167], v[172:175], v[90:93]
	v_mfma_f32_16x16x32_bf16 v[86:89], v[156:159], v[180:183], v[86:89]
	v_mfma_f32_16x16x32_bf16 v[82:85], v[164:167], v[180:183], v[82:85]
	v_mfma_f32_16x16x32_bf16 v[78:81], v[156:159], v[188:191], v[78:81]
	v_mfma_f32_16x16x32_bf16 v[74:77], v[164:167], v[188:191], v[74:77]
	v_mfma_f32_16x16x32_bf16 v[70:73], v[156:159], v[202:205], v[70:73]
	v_mfma_f32_16x16x32_bf16 v[66:69], v[164:167], v[202:205], v[66:69]
	v_mfma_f32_16x16x32_bf16 v[94:97], v[160:163], v[176:179], v[94:97]
	v_mfma_f32_16x16x32_bf16 v[90:93], v[168:171], v[176:179], v[90:93]
	v_mfma_f32_16x16x32_bf16 v[86:89], v[160:163], v[184:187], v[86:89]
	v_mfma_f32_16x16x32_bf16 v[82:85], v[168:171], v[184:187], v[82:85]
	v_mfma_f32_16x16x32_bf16 v[78:81], v[160:163], v[194:197], v[78:81]
	v_mfma_f32_16x16x32_bf16 v[74:77], v[168:171], v[194:197], v[74:77]
	v_mfma_f32_16x16x32_bf16 v[70:73], v[160:163], v[206:209], v[70:73]
	v_mfma_f32_16x16x32_bf16 v[66:69], v[168:171], v[206:209], v[66:69]
	s_setprio 0
	s_barrier
	ds_read_b128 v[172:175], v137 offset:49152
	ds_read_b128 v[176:179], v137 offset:50176
	ds_read_b128 v[180:183], v137 offset:51200
	ds_read_b128 v[184:187], v137 offset:52224
	ds_read_b128 v[188:191], v137 offset:53248
	ds_read_b128 v[194:197], v137 offset:54272
	ds_read_b128 v[202:205], v137 offset:55296
	ds_read_b128 v[206:209], v137 offset:56320
	s_add_u32 s34, s19, 0x180
	s_addc_u32 s35, s21, 0
	s_mov_b32 m0, s51
	s_nop 0
	global_load_lds_dwordx4 v114, s[34:35]
	s_nop 0
	s_mov_b32 m0, s52
	s_nop 0
	global_load_lds_dwordx4 v135, s[34:35]
	s_add_u32 s34, s19, 0x40180
	s_addc_u32 s35, s21, 0
	s_mov_b32 m0, s55
	s_nop 0
	global_load_lds_dwordx4 v114, s[34:35]
	s_nop 0
	s_mov_b32 m0, s56
	s_nop 0
	global_load_lds_dwordx4 v135, s[34:35]
	s_nop 0
	s_mov_b32 m0, s53
	s_nop 0
	global_load_lds_dwordx4 v65, s[26:27]
	s_nop 0
	s_mov_b32 m0, s54
	s_nop 0
	global_load_lds_dwordx4 v134, s[26:27]
	s_waitcnt vmcnt(8)
	s_waitcnt lgkmcnt(0)
	s_barrier
	s_setprio 1
	s_waitcnt lgkmcnt(0)
	v_mfma_f32_16x16x32_bf16 v[60:63], v[140:143], v[172:175], v[60:63]
	v_mfma_f32_16x16x32_bf16 v[56:59], v[148:151], v[172:175], v[56:59]
	s_waitcnt lgkmcnt(5)
	v_mfma_f32_16x16x32_bf16 v[52:55], v[140:143], v[180:183], v[52:55]
	v_mfma_f32_16x16x32_bf16 v[48:51], v[148:151], v[180:183], v[48:51]
	s_waitcnt lgkmcnt(3)
	v_mfma_f32_16x16x32_bf16 v[44:47], v[140:143], v[188:191], v[44:47]
	v_mfma_f32_16x16x32_bf16 v[40:43], v[148:151], v[188:191], v[40:43]
	s_waitcnt lgkmcnt(1)
	v_mfma_f32_16x16x32_bf16 v[36:39], v[140:143], v[202:205], v[36:39]
	v_mfma_f32_16x16x32_bf16 v[32:35], v[148:151], v[202:205], v[32:35]
	v_mfma_f32_16x16x32_bf16 v[60:63], v[144:147], v[176:179], v[60:63]
	v_mfma_f32_16x16x32_bf16 v[56:59], v[152:155], v[176:179], v[56:59]
	v_mfma_f32_16x16x32_bf16 v[52:55], v[144:147], v[184:187], v[52:55]
	v_mfma_f32_16x16x32_bf16 v[48:51], v[152:155], v[184:187], v[48:51]
	v_mfma_f32_16x16x32_bf16 v[44:47], v[144:147], v[194:197], v[44:47]
	v_mfma_f32_16x16x32_bf16 v[40:43], v[152:155], v[194:197], v[40:43]
	s_waitcnt lgkmcnt(0)
	v_mfma_f32_16x16x32_bf16 v[36:39], v[144:147], v[206:209], v[36:39]
	v_mfma_f32_16x16x32_bf16 v[32:35], v[152:155], v[206:209], v[32:35]
	s_setprio 0
	s_setprio 1
	v_mfma_f32_16x16x32_bf16 v[28:31], v[156:159], v[172:175], v[28:31]
	v_mfma_f32_16x16x32_bf16 v[24:27], v[164:167], v[172:175], v[24:27]
	v_mfma_f32_16x16x32_bf16 v[20:23], v[156:159], v[180:183], v[20:23]
	v_mfma_f32_16x16x32_bf16 v[16:19], v[164:167], v[180:183], v[16:19]
	v_mfma_f32_16x16x32_bf16 v[12:15], v[156:159], v[188:191], v[12:15]
	v_mfma_f32_16x16x32_bf16 v[8:11], v[164:167], v[188:191], v[8:11]
	v_mfma_f32_16x16x32_bf16 v[4:7], v[156:159], v[202:205], v[4:7]
	v_mfma_f32_16x16x32_bf16 v[0:3], v[164:167], v[202:205], v[0:3]
	v_mfma_f32_16x16x32_bf16 v[28:31], v[160:163], v[176:179], v[28:31]
	v_mfma_f32_16x16x32_bf16 v[24:27], v[168:171], v[176:179], v[24:27]
	v_mfma_f32_16x16x32_bf16 v[20:23], v[160:163], v[184:187], v[20:23]
	v_mfma_f32_16x16x32_bf16 v[16:19], v[168:171], v[184:187], v[16:19]
	v_mfma_f32_16x16x32_bf16 v[12:15], v[160:163], v[194:197], v[12:15]
	v_mfma_f32_16x16x32_bf16 v[8:11], v[168:171], v[194:197], v[8:11]
	v_mfma_f32_16x16x32_bf16 v[4:7], v[160:163], v[206:209], v[4:7]
	v_mfma_f32_16x16x32_bf16 v[0:3], v[168:171], v[206:209], v[0:3]
	s_setprio 0
	s_barrier
	s_add_i32 s17, s17, 2
	s_add_u32 s2, s2, 0x100
	s_addc_u32 s3, s3, 0
	s_cmp_lt_u32 s17, 12

.LBB0_626:
	v_mov_b32_e32 v0, 0
	s_mov_b32 s13, -2
	s_mov_b64 s[2:3], 0
	v_mov_b32_e32 v1, v0
	s_waitcnt lgkmcnt(0)
	s_add_u32 s33, s24, s2
	s_addc_u32 s40, s25, s3
	v_add_u32_e32 v114, 0x10000, v143
	v_add_u32_e32 v133, 0x14000, v143
	s_add_u32 s18, s33, 0x100
	ds_read_b128 v[134:137], v114
	ds_read_b128 v[146:149], v114 offset:1024
	ds_read_b128 v[150:153], v114 offset:2048
	ds_read_b128 v[154:157], v114 offset:3072
	ds_read_b128 v[158:161], v133
	ds_read_b128 v[162:165], v133 offset:1024
	ds_read_b128 v[166:169], v133 offset:2048
	ds_read_b128 v[170:173], v133 offset:3072
	s_addc_u32 s19, s40, 0
	s_add_u32 s16, s33, 0x180
	s_addc_u32 s17, s40, 0
	s_add_u32 s15, s26, s2
	s_addc_u32 s23, s27, s3
	s_add_u32 s36, s15, 0x100
	s_addc_u32 s37, s23, 0
	ds_read_b128 v[174:177], v144
	ds_read_b128 v[178:181], v144 offset:1024
	ds_read_b128 v[182:185], v144 offset:2048
	ds_read_b128 v[186:189], v144 offset:3072
	ds_read_b128 v[202:205], v144 offset:4096
	ds_read_b128 v[206:209], v144 offset:5120
	ds_read_b128 v[210:213], v144 offset:6144
	ds_read_b128 v[214:217], v144 offset:7168
	s_add_u32 s38, s33, 0x40080
	s_addc_u32 s39, s40, 0
	s_mov_b32 m0, s60
	s_nop 0
	global_load_lds_dwordx4 v65, s[38:39]
	s_nop 0
	s_mov_b32 m0, s61
	s_nop 0
	global_load_lds_dwordx4 v141, s[38:39]
	s_waitcnt vmcnt(8)
	s_waitcnt lgkmcnt(0)
	s_barrier
	s_setprio 1
	s_waitcnt lgkmcnt(0)
	v_mfma_f32_16x16x32_bf16 v[128:131], v[134:137], v[174:177], 0
	v_mfma_f32_16x16x32_bf16 v[124:127], v[150:153], v[174:177], 0
	v_mfma_f32_16x16x32_bf16 v[120:123], v[134:137], v[182:185], 0
	v_mfma_f32_16x16x32_bf16 v[116:119], v[150:153], v[182:185], 0
	v_mfma_f32_16x16x32_bf16 v[110:113], v[134:137], v[202:205], 0
	v_mfma_f32_16x16x32_bf16 v[106:109], v[150:153], v[202:205], 0
	v_mfma_f32_16x16x32_bf16 v[102:105], v[134:137], v[210:213], 0
	v_mfma_f32_16x16x32_bf16 v[98:101], v[150:153], v[210:213], 0
	v_mfma_f32_16x16x32_bf16 v[128:131], v[146:149], v[178:181], v[128:131]
	v_mfma_f32_16x16x32_bf16 v[124:127], v[154:157], v[178:181], v[124:127]
	v_mfma_f32_16x16x32_bf16 v[120:123], v[146:149], v[186:189], v[120:123]
	v_mfma_f32_16x16x32_bf16 v[116:119], v[154:157], v[186:189], v[116:119]
	v_mfma_f32_16x16x32_bf16 v[110:113], v[146:149], v[206:209], v[110:113]
	v_mfma_f32_16x16x32_bf16 v[106:109], v[154:157], v[206:209], v[106:109]
	v_mfma_f32_16x16x32_bf16 v[102:105], v[146:149], v[214:217], v[102:105]
	v_mfma_f32_16x16x32_bf16 v[98:101], v[154:157], v[214:217], v[98:101]
	s_setprio 0
	s_setprio 1
	v_mfma_f32_16x16x32_bf16 v[94:97], v[158:161], v[174:177], 0
	v_mfma_f32_16x16x32_bf16 v[90:93], v[166:169], v[174:177], 0
	v_mfma_f32_16x16x32_bf16 v[86:89], v[158:161], v[182:185], 0
	v_mfma_f32_16x16x32_bf16 v[82:85], v[166:169], v[182:185], 0
	v_mfma_f32_16x16x32_bf16 v[78:81], v[158:161], v[202:205], 0
	v_mfma_f32_16x16x32_bf16 v[74:77], v[166:169], v[202:205], 0
	v_mfma_f32_16x16x32_bf16 v[70:73], v[158:161], v[210:213], 0
	v_mfma_f32_16x16x32_bf16 v[66:69], v[166:169], v[210:213], 0
	v_mfma_f32_16x16x32_bf16 v[94:97], v[162:165], v[178:181], v[94:97]
	v_mfma_f32_16x16x32_bf16 v[90:93], v[170:173], v[178:181], v[90:93]
	v_mfma_f32_16x16x32_bf16 v[86:89], v[162:165], v[186:189], v[86:89]
	v_mfma_f32_16x16x32_bf16 v[82:85], v[170:173], v[186:189], v[82:85]
	v_mfma_f32_16x16x32_bf16 v[78:81], v[162:165], v[206:209], v[78:81]
	v_mfma_f32_16x16x32_bf16 v[74:77], v[170:173], v[206:209], v[74:77]
	v_mfma_f32_16x16x32_bf16 v[70:73], v[162:165], v[214:217], v[70:73]
	v_mfma_f32_16x16x32_bf16 v[66:69], v[170:173], v[214:217], v[66:69]
	s_setprio 0
	s_barrier
	ds_read_b128 v[174:177], v144 offset:16384
	ds_read_b128 v[178:181], v144 offset:17408
	ds_read_b128 v[182:185], v144 offset:18432
	ds_read_b128 v[186:189], v144 offset:19456
	ds_read_b128 v[202:205], v144 offset:20480
	ds_read_b128 v[206:209], v144 offset:21504
	ds_read_b128 v[210:213], v144 offset:22528
	ds_read_b128 v[214:217], v144 offset:23552
	s_mov_b32 m0, s48
	s_nop 0
	global_load_lds_dwordx4 v140, s[36:37]
	s_nop 0
	s_mov_b32 m0, s49
	s_nop 0
	global_load_lds_dwordx4 v142, s[36:37]
	s_add_u32 s36, s15, 0x40100
	s_addc_u32 s37, s23, 0
	s_mov_b32 m0, s50
	s_nop 0
	global_load_lds_dwordx4 v140, s[36:37]
	s_nop 0
	s_mov_b32 m0, s51
	s_nop 0
	global_load_lds_dwordx4 v142, s[36:37]
	s_mov_b32 m0, s47
	s_nop 0
	global_load_lds_dwordx4 v65, s[18:19]
	s_nop 0
	s_mov_b32 m0, s52
	s_nop 0
	global_load_lds_dwordx4 v141, s[18:19]
	s_waitcnt vmcnt(8)
	s_waitcnt lgkmcnt(0)
	s_barrier
	s_setprio 1
	s_waitcnt lgkmcnt(0)
	v_mfma_f32_16x16x32_bf16 v[60:63], v[134:137], v[174:177], 0
	v_mfma_f32_16x16x32_bf16 v[56:59], v[150:153], v[174:177], 0
	s_waitcnt lgkmcnt(5)
	v_mfma_f32_16x16x32_bf16 v[52:55], v[134:137], v[182:185], 0
	v_mfma_f32_16x16x32_bf16 v[48:51], v[150:153], v[182:185], 0
	s_waitcnt lgkmcnt(3)
	v_mfma_f32_16x16x32_bf16 v[44:47], v[134:137], v[202:205], 0
	v_mfma_f32_16x16x32_bf16 v[40:43], v[150:153], v[202:205], 0
	s_waitcnt lgkmcnt(1)
	v_mfma_f32_16x16x32_bf16 v[36:39], v[134:137], v[210:213], 0
	v_mfma_f32_16x16x32_bf16 v[32:35], v[150:153], v[210:213], 0
	v_mfma_f32_16x16x32_bf16 v[60:63], v[146:149], v[178:181], v[60:63]
	v_mfma_f32_16x16x32_bf16 v[56:59], v[154:157], v[178:181], v[56:59]
	v_mfma_f32_16x16x32_bf16 v[52:55], v[146:149], v[186:189], v[52:55]
	v_mfma_f32_16x16x32_bf16 v[48:51], v[154:157], v[186:189], v[48:51]
	v_mfma_f32_16x16x32_bf16 v[44:47], v[146:149], v[206:209], v[44:47]
	v_mfma_f32_16x16x32_bf16 v[40:43], v[154:157], v[206:209], v[40:43]
	s_waitcnt lgkmcnt(0)
	v_mfma_f32_16x16x32_bf16 v[36:39], v[146:149], v[214:217], v[36:39]
	v_mfma_f32_16x16x32_bf16 v[32:35], v[154:157], v[214:217], v[32:35]
	s_setprio 0
	s_setprio 1
	v_mfma_f32_16x16x32_bf16 v[28:31], v[158:161], v[174:177], 0
	v_mfma_f32_16x16x32_bf16 v[24:27], v[166:169], v[174:177], 0
	v_mfma_f32_16x16x32_bf16 v[20:23], v[158:161], v[182:185], 0
	v_mfma_f32_16x16x32_bf16 v[16:19], v[166:169], v[182:185], 0
	v_mfma_f32_16x16x32_bf16 v[12:15], v[158:161], v[202:205], 0
	v_mfma_f32_16x16x32_bf16 v[8:11], v[166:169], v[202:205], 0
	v_mfma_f32_16x16x32_bf16 v[4:7], v[158:161], v[210:213], 0
	v_mfma_f32_16x16x32_bf16 v[0:3], v[166:169], v[210:213], 0
	v_mfma_f32_16x16x32_bf16 v[28:31], v[162:165], v[178:181], v[28:31]
	v_mfma_f32_16x16x32_bf16 v[24:27], v[170:173], v[178:181], v[24:27]
	v_mfma_f32_16x16x32_bf16 v[20:23], v[162:165], v[186:189], v[20:23]
	v_mfma_f32_16x16x32_bf16 v[16:19], v[170:173], v[186:189], v[16:19]
	v_mfma_f32_16x16x32_bf16 v[12:15], v[162:165], v[206:209], v[12:15]
	v_mfma_f32_16x16x32_bf16 v[8:11], v[170:173], v[206:209], v[8:11]
	v_mfma_f32_16x16x32_bf16 v[4:7], v[162:165], v[214:217], v[4:7]
	v_mfma_f32_16x16x32_bf16 v[0:3], v[170:173], v[214:217], v[0:3]
	s_setprio 0
	s_barrier
	v_add_u32_e32 v132, 0x18000, v143
	v_add_u32_e32 v134, 0x1c000, v143
	ds_read_b128 v[136:139], v132
	ds_read_b128 v[146:149], v132 offset:1024
	ds_read_b128 v[150:153], v132 offset:2048
	ds_read_b128 v[154:157], v132 offset:3072
	ds_read_b128 v[158:161], v134
	ds_read_b128 v[162:165], v134 offset:1024
	ds_read_b128 v[166:169], v134 offset:2048
	ds_read_b128 v[170:173], v134 offset:3072
	ds_read_b128 v[174:177], v144 offset:32768
	ds_read_b128 v[178:181], v144 offset:33792
	ds_read_b128 v[182:185], v144 offset:34816
	ds_read_b128 v[186:189], v144 offset:35840
	ds_read_b128 v[202:205], v144 offset:36864
	ds_read_b128 v[206:209], v144 offset:37888
	ds_read_b128 v[210:213], v144 offset:38912
	ds_read_b128 v[214:217], v144 offset:39936
	s_add_u32 s18, s33, 0x40100
	s_addc_u32 s19, s40, 0
	s_mov_b32 m0, s53
	s_nop 0
	global_load_lds_dwordx4 v65, s[18:19]
	s_nop 0
	s_mov_b32 m0, s54
	s_nop 0
	global_load_lds_dwordx4 v141, s[18:19]
	s_waitcnt vmcnt(8)
	s_waitcnt lgkmcnt(0)
	s_barrier
	s_setprio 1
	s_waitcnt lgkmcnt(0)
	v_mfma_f32_16x16x32_bf16 v[128:131], v[136:139], v[174:177], v[128:131]
	v_mfma_f32_16x16x32_bf16 v[124:127], v[150:153], v[174:177], v[124:127]
	s_waitcnt lgkmcnt(5)
	v_mfma_f32_16x16x32_bf16 v[120:123], v[136:139], v[182:185], v[120:123]
	v_mfma_f32_16x16x32_bf16 v[116:119], v[150:153], v[182:185], v[116:119]
	s_waitcnt lgkmcnt(3)
	v_mfma_f32_16x16x32_bf16 v[110:113], v[136:139], v[202:205], v[110:113]
	v_mfma_f32_16x16x32_bf16 v[106:109], v[150:153], v[202:205], v[106:109]
	s_waitcnt lgkmcnt(1)
	v_mfma_f32_16x16x32_bf16 v[102:105], v[136:139], v[210:213], v[102:105]
	v_mfma_f32_16x16x32_bf16 v[98:101], v[150:153], v[210:213], v[98:101]
	v_mfma_f32_16x16x32_bf16 v[128:131], v[146:149], v[178:181], v[128:131]
	v_mfma_f32_16x16x32_bf16 v[124:127], v[154:157], v[178:181], v[124:127]
	v_mfma_f32_16x16x32_bf16 v[120:123], v[146:149], v[186:189], v[120:123]
	v_mfma_f32_16x16x32_bf16 v[116:119], v[154:157], v[186:189], v[116:119]
	v_mfma_f32_16x16x32_bf16 v[110:113], v[146:149], v[206:209], v[110:113]
	v_mfma_f32_16x16x32_bf16 v[106:109], v[154:157], v[206:209], v[106:109]
	s_waitcnt lgkmcnt(0)
	v_mfma_f32_16x16x32_bf16 v[102:105], v[146:149], v[214:217], v[102:105]
	v_mfma_f32_16x16x32_bf16 v[98:101], v[154:157], v[214:217], v[98:101]
	s_setprio 0
	s_setprio 1
	v_mfma_f32_16x16x32_bf16 v[94:97], v[158:161], v[174:177], v[94:97]
	v_mfma_f32_16x16x32_bf16 v[90:93], v[166:169], v[174:177], v[90:93]
	v_mfma_f32_16x16x32_bf16 v[86:89], v[158:161], v[182:185], v[86:89]
	v_mfma_f32_16x16x32_bf16 v[82:85], v[166:169], v[182:185], v[82:85]
	v_mfma_f32_16x16x32_bf16 v[78:81], v[158:161], v[202:205], v[78:81]
	v_mfma_f32_16x16x32_bf16 v[74:77], v[166:169], v[202:205], v[74:77]
	v_mfma_f32_16x16x32_bf16 v[70:73], v[158:161], v[210:213], v[70:73]
	v_mfma_f32_16x16x32_bf16 v[66:69], v[166:169], v[210:213], v[66:69]
	v_mfma_f32_16x16x32_bf16 v[94:97], v[162:165], v[178:181], v[94:97]
	v_mfma_f32_16x16x32_bf16 v[90:93], v[170:173], v[178:181], v[90:93]
	v_mfma_f32_16x16x32_bf16 v[86:89], v[162:165], v[186:189], v[86:89]
	v_mfma_f32_16x16x32_bf16 v[82:85], v[170:173], v[186:189], v[82:85]
	v_mfma_f32_16x16x32_bf16 v[78:81], v[162:165], v[206:209], v[78:81]
	v_mfma_f32_16x16x32_bf16 v[74:77], v[170:173], v[206:209], v[74:77]
	v_mfma_f32_16x16x32_bf16 v[70:73], v[162:165], v[214:217], v[70:73]
	v_mfma_f32_16x16x32_bf16 v[66:69], v[170:173], v[214:217], v[66:69]
	s_setprio 0
	s_barrier
	ds_read_b128 v[174:177], v144 offset:49152
	ds_read_b128 v[178:181], v144 offset:50176
	ds_read_b128 v[182:185], v144 offset:51200
	ds_read_b128 v[186:189], v144 offset:52224
	ds_read_b128 v[202:205], v144 offset:53248
	ds_read_b128 v[206:209], v144 offset:54272
	ds_read_b128 v[210:213], v144 offset:55296
	ds_read_b128 v[214:217], v144 offset:56320
	s_add_u32 s18, s15, 0x180
	s_addc_u32 s19, s23, 0
	s_mov_b32 m0, s30
	s_nop 0
	global_load_lds_dwordx4 v140, s[18:19]
	s_nop 0
	s_mov_b32 m0, s55
	s_nop 0
	global_load_lds_dwordx4 v142, s[18:19]
	s_add_u32 s18, s15, 0x40180
	s_addc_u32 s19, s23, 0
	s_mov_b32 m0, s58
	s_nop 0
	global_load_lds_dwordx4 v140, s[18:19]
	s_nop 0
	s_mov_b32 m0, s59
	s_nop 0
	global_load_lds_dwordx4 v142, s[18:19]
	s_nop 0
	s_mov_b32 m0, s56
	s_nop 0
	global_load_lds_dwordx4 v65, s[16:17]
	s_nop 0
	s_mov_b32 m0, s57
	s_nop 0
	global_load_lds_dwordx4 v141, s[16:17]
	s_waitcnt vmcnt(8)
	s_waitcnt lgkmcnt(0)
	s_barrier
	s_setprio 1
	s_waitcnt lgkmcnt(0)
	v_mfma_f32_16x16x32_bf16 v[60:63], v[136:139], v[174:177], v[60:63]
	v_mfma_f32_16x16x32_bf16 v[56:59], v[150:153], v[174:177], v[56:59]
	s_waitcnt lgkmcnt(5)
	v_mfma_f32_16x16x32_bf16 v[52:55], v[136:139], v[182:185], v[52:55]
	v_mfma_f32_16x16x32_bf16 v[48:51], v[150:153], v[182:185], v[48:51]
	s_waitcnt lgkmcnt(3)
	v_mfma_f32_16x16x32_bf16 v[44:47], v[136:139], v[202:205], v[44:47]
	v_mfma_f32_16x16x32_bf16 v[40:43], v[150:153], v[202:205], v[40:43]
	s_waitcnt lgkmcnt(1)
	v_mfma_f32_16x16x32_bf16 v[36:39], v[136:139], v[210:213], v[36:39]
	v_mfma_f32_16x16x32_bf16 v[32:35], v[150:153], v[210:213], v[32:35]
	v_mfma_f32_16x16x32_bf16 v[60:63], v[146:149], v[178:181], v[60:63]
	v_mfma_f32_16x16x32_bf16 v[56:59], v[154:157], v[178:181], v[56:59]
	v_mfma_f32_16x16x32_bf16 v[52:55], v[146:149], v[186:189], v[52:55]
	v_mfma_f32_16x16x32_bf16 v[48:51], v[154:157], v[186:189], v[48:51]
	v_mfma_f32_16x16x32_bf16 v[44:47], v[146:149], v[206:209], v[44:47]
	v_mfma_f32_16x16x32_bf16 v[40:43], v[154:157], v[206:209], v[40:43]
	s_waitcnt lgkmcnt(0)
	v_mfma_f32_16x16x32_bf16 v[36:39], v[146:149], v[214:217], v[36:39]
	v_mfma_f32_16x16x32_bf16 v[32:35], v[154:157], v[214:217], v[32:35]
	s_setprio 0
	s_setprio 1
	v_mfma_f32_16x16x32_bf16 v[28:31], v[158:161], v[174:177], v[28:31]
	v_mfma_f32_16x16x32_bf16 v[24:27], v[166:169], v[174:177], v[24:27]
	v_mfma_f32_16x16x32_bf16 v[20:23], v[158:161], v[182:185], v[20:23]
	v_mfma_f32_16x16x32_bf16 v[16:19], v[166:169], v[182:185], v[16:19]
	v_mfma_f32_16x16x32_bf16 v[12:15], v[158:161], v[202:205], v[12:15]
	v_mfma_f32_16x16x32_bf16 v[8:11], v[166:169], v[202:205], v[8:11]
	v_mfma_f32_16x16x32_bf16 v[4:7], v[158:161], v[210:213], v[4:7]
	v_mfma_f32_16x16x32_bf16 v[0:3], v[166:169], v[210:213], v[0:3]
	v_mfma_f32_16x16x32_bf16 v[28:31], v[162:165], v[178:181], v[28:31]
	v_mfma_f32_16x16x32_bf16 v[24:27], v[170:173], v[178:181], v[24:27]
	v_mfma_f32_16x16x32_bf16 v[20:23], v[162:165], v[186:189], v[20:23]
	v_mfma_f32_16x16x32_bf16 v[16:19], v[170:173], v[186:189], v[16:19]
	v_mfma_f32_16x16x32_bf16 v[12:15], v[162:165], v[206:209], v[12:15]
	v_mfma_f32_16x16x32_bf16 v[8:11], v[170:173], v[206:209], v[8:11]
	v_mfma_f32_16x16x32_bf16 v[4:7], v[162:165], v[214:217], v[4:7]
	v_mfma_f32_16x16x32_bf16 v[0:3], v[170:173], v[214:217], v[0:3]
	s_setprio 0
	s_barrier
	s_add_i32 s13, s13, 2
	s_add_u32 s2, s2, 0x100
	s_addc_u32 s3, s3, 0
	s_cmp_lt_u32 s13, 12

.LBB0_1110:
	v_mov_b32_e32 v0, 0
	s_mov_b32 s15, -2
	s_mov_b64 s[2:3], 0
	v_mov_b32_e32 v1, v0
	s_waitcnt lgkmcnt(0)
	s_add_u32 s66, s26, s2
	s_addc_u32 s67, s27, s3
	s_nop 0
	v_add_u32_e32 v132, 0x10000, v204
	v_add_u32_e32 v134, 0x14000, v204
	s_add_u32 s20, s66, 0x100
	ds_read_b128 v[136:139], v132
	ds_read_b128 v[140:143], v132 offset:1024
	ds_read_b128 v[144:147], v132 offset:2048
	ds_read_b128 v[148:151], v132 offset:3072
	ds_read_b128 v[152:155], v134
	ds_read_b128 v[156:159], v134 offset:1024
	ds_read_b128 v[160:163], v134 offset:2048
	ds_read_b128 v[164:167], v134 offset:3072
	s_addc_u32 s21, s67, 0
	s_add_u32 s18, s66, 0x180
	s_addc_u32 s19, s67, 0
	s_add_u32 s17, s24, s2
	s_addc_u32 s33, s25, s3
	s_add_u32 s34, s17, 0x100
	s_addc_u32 s35, s33, 0
	ds_read_b128 v[168:171], v205
	ds_read_b128 v[172:175], v205 offset:1024
	ds_read_b128 v[176:179], v205 offset:2048
	ds_read_b128 v[180:183], v205 offset:3072
	ds_read_b128 v[184:187], v205 offset:4096
	ds_read_b128 v[188:191], v205 offset:5120
	ds_read_b128 v[194:197], v205 offset:6144
	ds_read_b128 v[198:201], v205 offset:7168
	s_add_u32 s64, s66, 0x40080
	s_addc_u32 s65, s67, 0
	s_mov_b32 m0, s62
	s_nop 0
	global_load_lds_dwordx4 v65, s[64:65]
	s_nop 0
	s_mov_b32 m0, s63
	s_nop 0
	global_load_lds_dwordx4 v202, s[64:65]
	s_waitcnt vmcnt(8)
	s_waitcnt lgkmcnt(0)
	s_barrier
	s_setprio 1
	s_waitcnt lgkmcnt(0)
	v_mfma_f32_16x16x32_bf16 v[128:131], v[136:139], v[168:171], 0
	v_mfma_f32_16x16x32_bf16 v[124:127], v[144:147], v[168:171], 0
	v_mfma_f32_16x16x32_bf16 v[120:123], v[136:139], v[176:179], 0
	v_mfma_f32_16x16x32_bf16 v[116:119], v[144:147], v[176:179], 0
	v_mfma_f32_16x16x32_bf16 v[110:113], v[136:139], v[184:187], 0
	v_mfma_f32_16x16x32_bf16 v[106:109], v[144:147], v[184:187], 0
	v_mfma_f32_16x16x32_bf16 v[102:105], v[136:139], v[194:197], 0
	v_mfma_f32_16x16x32_bf16 v[98:101], v[144:147], v[194:197], 0
	v_mfma_f32_16x16x32_bf16 v[128:131], v[140:143], v[172:175], v[128:131]
	v_mfma_f32_16x16x32_bf16 v[124:127], v[148:151], v[172:175], v[124:127]
	v_mfma_f32_16x16x32_bf16 v[120:123], v[140:143], v[180:183], v[120:123]
	v_mfma_f32_16x16x32_bf16 v[116:119], v[148:151], v[180:183], v[116:119]
	v_mfma_f32_16x16x32_bf16 v[110:113], v[140:143], v[188:191], v[110:113]
	v_mfma_f32_16x16x32_bf16 v[106:109], v[148:151], v[188:191], v[106:109]
	v_mfma_f32_16x16x32_bf16 v[102:105], v[140:143], v[198:201], v[102:105]
	v_mfma_f32_16x16x32_bf16 v[98:101], v[148:151], v[198:201], v[98:101]
	s_setprio 0
	s_setprio 1
	v_mfma_f32_16x16x32_bf16 v[94:97], v[152:155], v[168:171], 0
	v_mfma_f32_16x16x32_bf16 v[90:93], v[160:163], v[168:171], 0
	v_mfma_f32_16x16x32_bf16 v[86:89], v[152:155], v[176:179], 0
	v_mfma_f32_16x16x32_bf16 v[82:85], v[160:163], v[176:179], 0
	v_mfma_f32_16x16x32_bf16 v[78:81], v[152:155], v[184:187], 0
	v_mfma_f32_16x16x32_bf16 v[74:77], v[160:163], v[184:187], 0
	v_mfma_f32_16x16x32_bf16 v[70:73], v[152:155], v[194:197], 0
	v_mfma_f32_16x16x32_bf16 v[66:69], v[160:163], v[194:197], 0
	v_mfma_f32_16x16x32_bf16 v[94:97], v[156:159], v[172:175], v[94:97]
	v_mfma_f32_16x16x32_bf16 v[90:93], v[164:167], v[172:175], v[90:93]
	v_mfma_f32_16x16x32_bf16 v[86:89], v[156:159], v[180:183], v[86:89]
	v_mfma_f32_16x16x32_bf16 v[82:85], v[164:167], v[180:183], v[82:85]
	v_mfma_f32_16x16x32_bf16 v[78:81], v[156:159], v[188:191], v[78:81]
	v_mfma_f32_16x16x32_bf16 v[74:77], v[164:167], v[188:191], v[74:77]
	v_mfma_f32_16x16x32_bf16 v[70:73], v[156:159], v[198:201], v[70:73]
	v_mfma_f32_16x16x32_bf16 v[66:69], v[164:167], v[198:201], v[66:69]
	s_setprio 0
	s_barrier
	ds_read_b128 v[168:171], v205 offset:16384
	ds_read_b128 v[172:175], v205 offset:17408
	ds_read_b128 v[176:179], v205 offset:18432
	ds_read_b128 v[180:183], v205 offset:19456
	ds_read_b128 v[184:187], v205 offset:20480
	ds_read_b128 v[188:191], v205 offset:21504
	ds_read_b128 v[194:197], v205 offset:22528
	ds_read_b128 v[198:201], v205 offset:23552
	s_mov_b32 m0, s44
	s_nop 0
	global_load_lds_dwordx4 v114, s[34:35]
	s_nop 0
	s_mov_b32 m0, s45
	s_nop 0
	global_load_lds_dwordx4 v203, s[34:35]
	s_add_u32 s34, s17, 0x40100
	s_addc_u32 s35, s33, 0
	s_mov_b32 m0, s46
	s_nop 0
	global_load_lds_dwordx4 v114, s[34:35]
	s_nop 0
	s_mov_b32 m0, s47
	s_nop 0
	global_load_lds_dwordx4 v203, s[34:35]
	s_mov_b32 m0, s43
	s_nop 0
	global_load_lds_dwordx4 v65, s[20:21]
	s_nop 0
	s_mov_b32 m0, s48
	s_nop 0
	global_load_lds_dwordx4 v202, s[20:21]
	s_waitcnt vmcnt(8)
	s_waitcnt lgkmcnt(0)
	s_barrier
	s_setprio 1
	s_waitcnt lgkmcnt(7)
	v_mfma_f32_16x16x32_bf16 v[60:63], v[136:139], v[168:171], 0
	v_mfma_f32_16x16x32_bf16 v[56:59], v[144:147], v[168:171], 0
	s_waitcnt lgkmcnt(5)
	v_mfma_f32_16x16x32_bf16 v[52:55], v[136:139], v[176:179], 0
	v_mfma_f32_16x16x32_bf16 v[48:51], v[144:147], v[176:179], 0
	s_waitcnt lgkmcnt(3)
	v_mfma_f32_16x16x32_bf16 v[44:47], v[136:139], v[184:187], 0
	v_mfma_f32_16x16x32_bf16 v[40:43], v[144:147], v[184:187], 0
	s_waitcnt lgkmcnt(1)
	v_mfma_f32_16x16x32_bf16 v[36:39], v[136:139], v[194:197], 0
	v_mfma_f32_16x16x32_bf16 v[32:35], v[144:147], v[194:197], 0
	v_mfma_f32_16x16x32_bf16 v[60:63], v[140:143], v[172:175], v[60:63]
	v_mfma_f32_16x16x32_bf16 v[56:59], v[148:151], v[172:175], v[56:59]
	v_mfma_f32_16x16x32_bf16 v[52:55], v[140:143], v[180:183], v[52:55]
	v_mfma_f32_16x16x32_bf16 v[48:51], v[148:151], v[180:183], v[48:51]
	v_mfma_f32_16x16x32_bf16 v[44:47], v[140:143], v[188:191], v[44:47]
	v_mfma_f32_16x16x32_bf16 v[40:43], v[148:151], v[188:191], v[40:43]
	s_waitcnt lgkmcnt(0)
	v_mfma_f32_16x16x32_bf16 v[36:39], v[140:143], v[198:201], v[36:39]
	v_mfma_f32_16x16x32_bf16 v[32:35], v[148:151], v[198:201], v[32:35]
	s_setprio 0
	s_setprio 1
	v_mfma_f32_16x16x32_bf16 v[28:31], v[152:155], v[168:171], 0
	v_mfma_f32_16x16x32_bf16 v[24:27], v[160:163], v[168:171], 0
	v_mfma_f32_16x16x32_bf16 v[20:23], v[152:155], v[176:179], 0
	v_mfma_f32_16x16x32_bf16 v[16:19], v[160:163], v[176:179], 0
	v_mfma_f32_16x16x32_bf16 v[12:15], v[152:155], v[184:187], 0
	v_mfma_f32_16x16x32_bf16 v[8:11], v[160:163], v[184:187], 0
	v_mfma_f32_16x16x32_bf16 v[4:7], v[152:155], v[194:197], 0
	v_mfma_f32_16x16x32_bf16 v[0:3], v[160:163], v[194:197], 0
	v_mfma_f32_16x16x32_bf16 v[28:31], v[156:159], v[172:175], v[28:31]
	v_mfma_f32_16x16x32_bf16 v[24:27], v[164:167], v[172:175], v[24:27]
	v_mfma_f32_16x16x32_bf16 v[20:23], v[156:159], v[180:183], v[20:23]
	v_mfma_f32_16x16x32_bf16 v[16:19], v[164:167], v[180:183], v[16:19]
	v_mfma_f32_16x16x32_bf16 v[12:15], v[156:159], v[188:191], v[12:15]
	v_mfma_f32_16x16x32_bf16 v[8:11], v[164:167], v[188:191], v[8:11]
	v_mfma_f32_16x16x32_bf16 v[4:7], v[156:159], v[198:201], v[4:7]
	v_mfma_f32_16x16x32_bf16 v[0:3], v[164:167], v[198:201], v[0:3]
	s_setprio 0
	s_barrier
	v_add_u32_e32 v133, 0x18000, v204
	v_add_u32_e32 v135, 0x1c000, v204
	ds_read_b128 v[136:139], v133
	ds_read_b128 v[140:143], v133 offset:1024
	ds_read_b128 v[144:147], v133 offset:2048
	ds_read_b128 v[148:151], v133 offset:3072
	ds_read_b128 v[152:155], v135
	ds_read_b128 v[156:159], v135 offset:1024
	ds_read_b128 v[160:163], v135 offset:2048
	ds_read_b128 v[164:167], v135 offset:3072
	ds_read_b128 v[168:171], v205 offset:32768
	ds_read_b128 v[172:175], v205 offset:33792
	ds_read_b128 v[176:179], v205 offset:34816
	ds_read_b128 v[180:183], v205 offset:35840
	ds_read_b128 v[184:187], v205 offset:36864
	ds_read_b128 v[188:191], v205 offset:37888
	ds_read_b128 v[194:197], v205 offset:38912
	ds_read_b128 v[198:201], v205 offset:39936
	s_add_u32 s20, s66, 0x40100
	s_addc_u32 s21, s67, 0
	s_mov_b32 m0, s49
	s_nop 0
	global_load_lds_dwordx4 v65, s[20:21]
	s_nop 0
	s_mov_b32 m0, s50
	s_nop 0
	global_load_lds_dwordx4 v202, s[20:21]
	s_waitcnt vmcnt(8)
	s_waitcnt lgkmcnt(0)
	s_barrier
	s_setprio 1
	s_waitcnt lgkmcnt(7)
	v_mfma_f32_16x16x32_bf16 v[128:131], v[136:139], v[168:171], v[128:131]
	v_mfma_f32_16x16x32_bf16 v[124:127], v[144:147], v[168:171], v[124:127]
	s_waitcnt lgkmcnt(5)
	v_mfma_f32_16x16x32_bf16 v[120:123], v[136:139], v[176:179], v[120:123]
	v_mfma_f32_16x16x32_bf16 v[116:119], v[144:147], v[176:179], v[116:119]
	s_waitcnt lgkmcnt(3)
	v_mfma_f32_16x16x32_bf16 v[110:113], v[136:139], v[184:187], v[110:113]
	v_mfma_f32_16x16x32_bf16 v[106:109], v[144:147], v[184:187], v[106:109]
	s_waitcnt lgkmcnt(1)
	v_mfma_f32_16x16x32_bf16 v[102:105], v[136:139], v[194:197], v[102:105]
	v_mfma_f32_16x16x32_bf16 v[98:101], v[144:147], v[194:197], v[98:101]
	v_mfma_f32_16x16x32_bf16 v[128:131], v[140:143], v[172:175], v[128:131]
	v_mfma_f32_16x16x32_bf16 v[124:127], v[148:151], v[172:175], v[124:127]
	v_mfma_f32_16x16x32_bf16 v[120:123], v[140:143], v[180:183], v[120:123]
	v_mfma_f32_16x16x32_bf16 v[116:119], v[148:151], v[180:183], v[116:119]
	v_mfma_f32_16x16x32_bf16 v[110:113], v[140:143], v[188:191], v[110:113]
	v_mfma_f32_16x16x32_bf16 v[106:109], v[148:151], v[188:191], v[106:109]
	s_waitcnt lgkmcnt(0)
	v_mfma_f32_16x16x32_bf16 v[102:105], v[140:143], v[198:201], v[102:105]
	v_mfma_f32_16x16x32_bf16 v[98:101], v[148:151], v[198:201], v[98:101]
	s_setprio 0
	s_setprio 1
	v_mfma_f32_16x16x32_bf16 v[94:97], v[152:155], v[168:171], v[94:97]
	v_mfma_f32_16x16x32_bf16 v[90:93], v[160:163], v[168:171], v[90:93]
	v_mfma_f32_16x16x32_bf16 v[86:89], v[152:155], v[176:179], v[86:89]
	v_mfma_f32_16x16x32_bf16 v[82:85], v[160:163], v[176:179], v[82:85]
	v_mfma_f32_16x16x32_bf16 v[78:81], v[152:155], v[184:187], v[78:81]
	v_mfma_f32_16x16x32_bf16 v[74:77], v[160:163], v[184:187], v[74:77]
	v_mfma_f32_16x16x32_bf16 v[70:73], v[152:155], v[194:197], v[70:73]
	v_mfma_f32_16x16x32_bf16 v[66:69], v[160:163], v[194:197], v[66:69]
	v_mfma_f32_16x16x32_bf16 v[94:97], v[156:159], v[172:175], v[94:97]
	v_mfma_f32_16x16x32_bf16 v[90:93], v[164:167], v[172:175], v[90:93]
	v_mfma_f32_16x16x32_bf16 v[86:89], v[156:159], v[180:183], v[86:89]
	v_mfma_f32_16x16x32_bf16 v[82:85], v[164:167], v[180:183], v[82:85]
	v_mfma_f32_16x16x32_bf16 v[78:81], v[156:159], v[188:191], v[78:81]
	v_mfma_f32_16x16x32_bf16 v[74:77], v[164:167], v[188:191], v[74:77]
	v_mfma_f32_16x16x32_bf16 v[70:73], v[156:159], v[198:201], v[70:73]
	v_mfma_f32_16x16x32_bf16 v[66:69], v[164:167], v[198:201], v[66:69]
	s_setprio 0
	s_barrier
	ds_read_b128 v[168:171], v205 offset:49152
	ds_read_b128 v[172:175], v205 offset:50176
	ds_read_b128 v[176:179], v205 offset:51200
	ds_read_b128 v[180:183], v205 offset:52224
	ds_read_b128 v[184:187], v205 offset:53248
	ds_read_b128 v[188:191], v205 offset:54272
	ds_read_b128 v[194:197], v205 offset:55296
	ds_read_b128 v[198:201], v205 offset:56320
	s_add_u32 s20, s17, 0x180
	s_addc_u32 s21, s33, 0
	s_mov_b32 m0, s56
	s_nop 0
	global_load_lds_dwordx4 v114, s[20:21]
	s_nop 0
	s_mov_b32 m0, s57
	s_nop 0
	global_load_lds_dwordx4 v203, s[20:21]
	s_add_u32 s20, s17, 0x40180
	s_addc_u32 s21, s33, 0
	s_mov_b32 m0, s60
	s_nop 0
	global_load_lds_dwordx4 v114, s[20:21]
	s_nop 0
	s_mov_b32 m0, s61
	s_nop 0
	global_load_lds_dwordx4 v203, s[20:21]
	s_nop 0
	s_mov_b32 m0, s58
	s_nop 0
	global_load_lds_dwordx4 v65, s[18:19]
	s_nop 0
	s_mov_b32 m0, s59
	s_nop 0
	global_load_lds_dwordx4 v202, s[18:19]
	s_waitcnt vmcnt(8)
	s_waitcnt lgkmcnt(0)
	s_barrier
	s_setprio 1
	s_waitcnt lgkmcnt(7)
	v_mfma_f32_16x16x32_bf16 v[60:63], v[136:139], v[168:171], v[60:63]
	v_mfma_f32_16x16x32_bf16 v[56:59], v[144:147], v[168:171], v[56:59]
	s_waitcnt lgkmcnt(5)
	v_mfma_f32_16x16x32_bf16 v[52:55], v[136:139], v[176:179], v[52:55]
	v_mfma_f32_16x16x32_bf16 v[48:51], v[144:147], v[176:179], v[48:51]
	s_waitcnt lgkmcnt(3)
	v_mfma_f32_16x16x32_bf16 v[44:47], v[136:139], v[184:187], v[44:47]
	v_mfma_f32_16x16x32_bf16 v[40:43], v[144:147], v[184:187], v[40:43]
	s_waitcnt lgkmcnt(1)
	v_mfma_f32_16x16x32_bf16 v[36:39], v[136:139], v[194:197], v[36:39]
	v_mfma_f32_16x16x32_bf16 v[32:35], v[144:147], v[194:197], v[32:35]
	v_mfma_f32_16x16x32_bf16 v[60:63], v[140:143], v[172:175], v[60:63]
	v_mfma_f32_16x16x32_bf16 v[56:59], v[148:151], v[172:175], v[56:59]
	v_mfma_f32_16x16x32_bf16 v[52:55], v[140:143], v[180:183], v[52:55]
	v_mfma_f32_16x16x32_bf16 v[48:51], v[148:151], v[180:183], v[48:51]
	v_mfma_f32_16x16x32_bf16 v[44:47], v[140:143], v[188:191], v[44:47]
	v_mfma_f32_16x16x32_bf16 v[40:43], v[148:151], v[188:191], v[40:43]
	s_waitcnt lgkmcnt(0)
	v_mfma_f32_16x16x32_bf16 v[36:39], v[140:143], v[198:201], v[36:39]
	v_mfma_f32_16x16x32_bf16 v[32:35], v[148:151], v[198:201], v[32:35]
	s_setprio 0
	s_setprio 1
	v_mfma_f32_16x16x32_bf16 v[28:31], v[152:155], v[168:171], v[28:31]
	v_mfma_f32_16x16x32_bf16 v[24:27], v[160:163], v[168:171], v[24:27]
	v_mfma_f32_16x16x32_bf16 v[20:23], v[152:155], v[176:179], v[20:23]
	v_mfma_f32_16x16x32_bf16 v[16:19], v[160:163], v[176:179], v[16:19]
	v_mfma_f32_16x16x32_bf16 v[12:15], v[152:155], v[184:187], v[12:15]
	v_mfma_f32_16x16x32_bf16 v[8:11], v[160:163], v[184:187], v[8:11]
	v_mfma_f32_16x16x32_bf16 v[4:7], v[152:155], v[194:197], v[4:7]
	v_mfma_f32_16x16x32_bf16 v[0:3], v[160:163], v[194:197], v[0:3]
	v_mfma_f32_16x16x32_bf16 v[28:31], v[156:159], v[172:175], v[28:31]
	v_mfma_f32_16x16x32_bf16 v[24:27], v[164:167], v[172:175], v[24:27]
	v_mfma_f32_16x16x32_bf16 v[20:23], v[156:159], v[180:183], v[20:23]
	v_mfma_f32_16x16x32_bf16 v[16:19], v[164:167], v[180:183], v[16:19]
	v_mfma_f32_16x16x32_bf16 v[12:15], v[156:159], v[188:191], v[12:15]
	v_mfma_f32_16x16x32_bf16 v[8:11], v[164:167], v[188:191], v[8:11]
	v_mfma_f32_16x16x32_bf16 v[4:7], v[156:159], v[198:201], v[4:7]
	v_mfma_f32_16x16x32_bf16 v[0:3], v[164:167], v[198:201], v[0:3]
	s_setprio 0
	s_barrier
	s_add_i32 s15, s15, 2
	s_add_u32 s2, s2, 0x100
	s_addc_u32 s3, s3, 0
	s_cmp_lt_u32 s15, 12

.LBB0_1424:
	v_mov_b32_e32 v0, 0
	v_readlane_b32 s72, v254, 62
	s_mov_b32 s21, -2
	s_mov_b64 s[2:3], 0
	v_mov_b32_e32 v1, v0
	v_readlane_b32 s73, v254, 63
	s_add_u32 s66, s72, s2
	s_addc_u32 s67, s73, s3
	s_add_u32 s34, s66, 0x2000100
	s_addc_u32 s35, s67, 0
	v_add_u32_e32 v141, 0x10000, v134
	v_add_u32_e32 v142, 0x14000, v134
	s_add_u32 s26, s66, 0x2000180
	ds_read_b128 v[144:147], v141
	ds_read_b128 v[148:151], v141 offset:1024
	ds_read_b128 v[152:155], v141 offset:2048
	ds_read_b128 v[156:159], v141 offset:3072
	ds_read_b128 v[160:163], v142
	ds_read_b128 v[164:167], v142 offset:1024
	ds_read_b128 v[168:171], v142 offset:2048
	ds_read_b128 v[172:175], v142 offset:3072
	s_addc_u32 s27, s67, 0
	s_add_u32 s33, s24, s2
	s_addc_u32 s63, s25, s3
	s_add_u32 s64, s33, 0x100
	s_addc_u32 s65, s63, 0
	s_add_u32 s66, s66, 0x2000080
	s_addc_u32 s67, s67, 0
	ds_read_b128 v[176:179], v135
	ds_read_b128 v[180:183], v135 offset:1024
	ds_read_b128 v[184:187], v135 offset:2048
	ds_read_b128 v[188:191], v135 offset:3072
	ds_read_b128 v[194:197], v135 offset:4096
	ds_read_b128 v[198:201], v135 offset:5120
	ds_read_b128 v[202:205], v135 offset:6144
	ds_read_b128 v[206:209], v135 offset:7168
	s_mov_b32 m0, s57
	s_nop 0
	global_load_lds_dwordx4 v133, s[66:67]
	s_nop 0
	s_mov_b32 m0, s58
	s_nop 0
	global_load_lds_dwordx4 v132, s[66:67]
	s_waitcnt vmcnt(8)
	s_waitcnt lgkmcnt(0)
	s_barrier
	s_setprio 1
	s_waitcnt lgkmcnt(0)
	v_mfma_f32_16x16x32_bf16 v[128:131], v[144:147], v[176:179], 0
	v_mfma_f32_16x16x32_bf16 v[124:127], v[152:155], v[176:179], 0
	s_waitcnt lgkmcnt(5)
	v_mfma_f32_16x16x32_bf16 v[120:123], v[144:147], v[184:187], 0
	v_mfma_f32_16x16x32_bf16 v[116:119], v[152:155], v[184:187], 0
	s_waitcnt lgkmcnt(3)
	v_mfma_f32_16x16x32_bf16 v[110:113], v[144:147], v[194:197], 0
	v_mfma_f32_16x16x32_bf16 v[106:109], v[152:155], v[194:197], 0
	s_waitcnt lgkmcnt(1)
	v_mfma_f32_16x16x32_bf16 v[102:105], v[144:147], v[202:205], 0
	v_mfma_f32_16x16x32_bf16 v[98:101], v[152:155], v[202:205], 0
	v_mfma_f32_16x16x32_bf16 v[128:131], v[148:151], v[180:183], v[128:131]
	v_mfma_f32_16x16x32_bf16 v[124:127], v[156:159], v[180:183], v[124:127]
	v_mfma_f32_16x16x32_bf16 v[120:123], v[148:151], v[188:191], v[120:123]
	v_mfma_f32_16x16x32_bf16 v[116:119], v[156:159], v[188:191], v[116:119]
	v_mfma_f32_16x16x32_bf16 v[110:113], v[148:151], v[198:201], v[110:113]
	v_mfma_f32_16x16x32_bf16 v[106:109], v[156:159], v[198:201], v[106:109]
	s_waitcnt lgkmcnt(0)
	v_mfma_f32_16x16x32_bf16 v[102:105], v[148:151], v[206:209], v[102:105]
	v_mfma_f32_16x16x32_bf16 v[98:101], v[156:159], v[206:209], v[98:101]
	s_setprio 0
	s_setprio 1
	v_mfma_f32_16x16x32_bf16 v[94:97], v[160:163], v[176:179], 0
	v_mfma_f32_16x16x32_bf16 v[90:93], v[168:171], v[176:179], 0
	v_mfma_f32_16x16x32_bf16 v[86:89], v[160:163], v[184:187], 0
	v_mfma_f32_16x16x32_bf16 v[82:85], v[168:171], v[184:187], 0
	v_mfma_f32_16x16x32_bf16 v[78:81], v[160:163], v[194:197], 0
	v_mfma_f32_16x16x32_bf16 v[74:77], v[168:171], v[194:197], 0
	v_mfma_f32_16x16x32_bf16 v[70:73], v[160:163], v[202:205], 0
	v_mfma_f32_16x16x32_bf16 v[66:69], v[168:171], v[202:205], 0
	v_mfma_f32_16x16x32_bf16 v[94:97], v[164:167], v[180:183], v[94:97]
	v_mfma_f32_16x16x32_bf16 v[90:93], v[172:175], v[180:183], v[90:93]
	v_mfma_f32_16x16x32_bf16 v[86:89], v[164:167], v[188:191], v[86:89]
	v_mfma_f32_16x16x32_bf16 v[82:85], v[172:175], v[188:191], v[82:85]
	v_mfma_f32_16x16x32_bf16 v[78:81], v[164:167], v[198:201], v[78:81]
	v_mfma_f32_16x16x32_bf16 v[74:77], v[172:175], v[198:201], v[74:77]
	v_mfma_f32_16x16x32_bf16 v[70:73], v[164:167], v[206:209], v[70:73]
	v_mfma_f32_16x16x32_bf16 v[66:69], v[172:175], v[206:209], v[66:69]
	s_setprio 0
	s_barrier
	ds_read_b128 v[176:179], v135 offset:16384
	ds_read_b128 v[180:183], v135 offset:17408
	ds_read_b128 v[184:187], v135 offset:18432
	ds_read_b128 v[188:191], v135 offset:19456
	ds_read_b128 v[194:197], v135 offset:20480
	ds_read_b128 v[198:201], v135 offset:21504
	ds_read_b128 v[202:205], v135 offset:22528
	ds_read_b128 v[206:209], v135 offset:23552
	s_mov_b32 m0, s41
	s_nop 0
	global_load_lds_dwordx4 v65, s[64:65]
	s_nop 0
	s_mov_b32 m0, s42
	s_nop 0
	global_load_lds_dwordx4 v114, s[64:65]
	s_add_u32 s64, s33, 0x40100
	s_addc_u32 s65, s63, 0
	s_mov_b32 m0, s43
	s_nop 0
	global_load_lds_dwordx4 v65, s[64:65]
	s_nop 0
	s_mov_b32 m0, s44
	s_nop 0
	global_load_lds_dwordx4 v114, s[64:65]
	s_mov_b32 m0, s40
	s_nop 0
	global_load_lds_dwordx4 v139, s[34:35]
	s_nop 0
	s_mov_b32 m0, s45
	s_nop 0
	global_load_lds_dwordx4 v138, s[34:35]
	s_waitcnt vmcnt(8)
	s_waitcnt lgkmcnt(0)
	s_barrier
	s_setprio 1
	s_waitcnt lgkmcnt(0)
	v_mfma_f32_16x16x32_bf16 v[60:63], v[144:147], v[176:179], 0
	v_mfma_f32_16x16x32_bf16 v[56:59], v[152:155], v[176:179], 0
	s_waitcnt lgkmcnt(5)
	v_mfma_f32_16x16x32_bf16 v[52:55], v[144:147], v[184:187], 0
	v_mfma_f32_16x16x32_bf16 v[48:51], v[152:155], v[184:187], 0
	s_waitcnt lgkmcnt(3)
	v_mfma_f32_16x16x32_bf16 v[44:47], v[144:147], v[194:197], 0
	v_mfma_f32_16x16x32_bf16 v[40:43], v[152:155], v[194:197], 0
	s_waitcnt lgkmcnt(1)
	v_mfma_f32_16x16x32_bf16 v[36:39], v[144:147], v[202:205], 0
	v_mfma_f32_16x16x32_bf16 v[32:35], v[152:155], v[202:205], 0
	v_mfma_f32_16x16x32_bf16 v[60:63], v[148:151], v[180:183], v[60:63]
	v_mfma_f32_16x16x32_bf16 v[56:59], v[156:159], v[180:183], v[56:59]
	v_mfma_f32_16x16x32_bf16 v[52:55], v[148:151], v[188:191], v[52:55]
	v_mfma_f32_16x16x32_bf16 v[48:51], v[156:159], v[188:191], v[48:51]
	v_mfma_f32_16x16x32_bf16 v[44:47], v[148:151], v[198:201], v[44:47]
	v_mfma_f32_16x16x32_bf16 v[40:43], v[156:159], v[198:201], v[40:43]
	s_waitcnt lgkmcnt(0)
	v_mfma_f32_16x16x32_bf16 v[36:39], v[148:151], v[206:209], v[36:39]
	v_mfma_f32_16x16x32_bf16 v[32:35], v[156:159], v[206:209], v[32:35]
	s_setprio 0
	s_setprio 1
	v_mfma_f32_16x16x32_bf16 v[28:31], v[160:163], v[176:179], 0
	v_mfma_f32_16x16x32_bf16 v[24:27], v[168:171], v[176:179], 0
	v_mfma_f32_16x16x32_bf16 v[20:23], v[160:163], v[184:187], 0
	v_mfma_f32_16x16x32_bf16 v[16:19], v[168:171], v[184:187], 0
	v_mfma_f32_16x16x32_bf16 v[12:15], v[160:163], v[194:197], 0
	v_mfma_f32_16x16x32_bf16 v[8:11], v[168:171], v[194:197], 0
	v_mfma_f32_16x16x32_bf16 v[4:7], v[160:163], v[202:205], 0
	v_mfma_f32_16x16x32_bf16 v[0:3], v[168:171], v[202:205], 0
	v_mfma_f32_16x16x32_bf16 v[28:31], v[164:167], v[180:183], v[28:31]
	v_mfma_f32_16x16x32_bf16 v[24:27], v[172:175], v[180:183], v[24:27]
	v_mfma_f32_16x16x32_bf16 v[20:23], v[164:167], v[188:191], v[20:23]
	v_mfma_f32_16x16x32_bf16 v[16:19], v[172:175], v[188:191], v[16:19]
	v_mfma_f32_16x16x32_bf16 v[12:15], v[164:167], v[198:201], v[12:15]
	v_mfma_f32_16x16x32_bf16 v[8:11], v[172:175], v[198:201], v[8:11]
	v_mfma_f32_16x16x32_bf16 v[4:7], v[164:167], v[206:209], v[4:7]
	v_mfma_f32_16x16x32_bf16 v[0:3], v[172:175], v[206:209], v[0:3]
	s_setprio 0
	s_barrier
	v_add_u32_e32 v143, 0x18000, v134
	v_add_u32_e32 v144, 0x1c000, v134
	ds_read_b128 v[146:149], v143
	ds_read_b128 v[150:153], v143 offset:1024
	ds_read_b128 v[154:157], v143 offset:2048
	ds_read_b128 v[158:161], v143 offset:3072
	ds_read_b128 v[162:165], v144
	ds_read_b128 v[166:169], v144 offset:1024
	ds_read_b128 v[170:173], v144 offset:2048
	ds_read_b128 v[174:177], v144 offset:3072
	ds_read_b128 v[178:181], v135 offset:32768
	ds_read_b128 v[182:185], v135 offset:33792
	ds_read_b128 v[186:189], v135 offset:34816
	ds_read_b128 v[194:197], v135 offset:35840
	ds_read_b128 v[198:201], v135 offset:36864
	ds_read_b128 v[202:205], v135 offset:37888
	ds_read_b128 v[206:209], v135 offset:38912
	ds_read_b128 v[210:213], v135 offset:39936
	s_mov_b32 m0, s46
	s_nop 0
	global_load_lds_dwordx4 v133, s[34:35]
	s_nop 0
	s_mov_b32 m0, s47
	s_nop 0
	global_load_lds_dwordx4 v132, s[34:35]
	s_waitcnt vmcnt(8)
	s_waitcnt lgkmcnt(0)
	s_barrier
	s_setprio 1
	s_waitcnt lgkmcnt(0)
	v_mfma_f32_16x16x32_bf16 v[128:131], v[146:149], v[178:181], v[128:131]
	v_mfma_f32_16x16x32_bf16 v[124:127], v[154:157], v[178:181], v[124:127]
	s_waitcnt lgkmcnt(5)
	v_mfma_f32_16x16x32_bf16 v[120:123], v[146:149], v[186:189], v[120:123]
	v_mfma_f32_16x16x32_bf16 v[116:119], v[154:157], v[186:189], v[116:119]
	s_waitcnt lgkmcnt(3)
	v_mfma_f32_16x16x32_bf16 v[110:113], v[146:149], v[198:201], v[110:113]
	v_mfma_f32_16x16x32_bf16 v[106:109], v[154:157], v[198:201], v[106:109]
	s_waitcnt lgkmcnt(1)
	v_mfma_f32_16x16x32_bf16 v[102:105], v[146:149], v[206:209], v[102:105]
	v_mfma_f32_16x16x32_bf16 v[98:101], v[154:157], v[206:209], v[98:101]
	v_mfma_f32_16x16x32_bf16 v[128:131], v[150:153], v[182:185], v[128:131]
	v_mfma_f32_16x16x32_bf16 v[124:127], v[158:161], v[182:185], v[124:127]
	v_mfma_f32_16x16x32_bf16 v[120:123], v[150:153], v[194:197], v[120:123]
	v_mfma_f32_16x16x32_bf16 v[116:119], v[158:161], v[194:197], v[116:119]
	v_mfma_f32_16x16x32_bf16 v[110:113], v[150:153], v[202:205], v[110:113]
	v_mfma_f32_16x16x32_bf16 v[106:109], v[158:161], v[202:205], v[106:109]
	s_waitcnt lgkmcnt(0)
	v_mfma_f32_16x16x32_bf16 v[102:105], v[150:153], v[210:213], v[102:105]
	v_mfma_f32_16x16x32_bf16 v[98:101], v[158:161], v[210:213], v[98:101]
	s_setprio 0
	s_setprio 1
	v_mfma_f32_16x16x32_bf16 v[94:97], v[162:165], v[178:181], v[94:97]
	v_mfma_f32_16x16x32_bf16 v[90:93], v[170:173], v[178:181], v[90:93]
	v_mfma_f32_16x16x32_bf16 v[86:89], v[162:165], v[186:189], v[86:89]
	v_mfma_f32_16x16x32_bf16 v[82:85], v[170:173], v[186:189], v[82:85]
	v_mfma_f32_16x16x32_bf16 v[78:81], v[162:165], v[198:201], v[78:81]
	v_mfma_f32_16x16x32_bf16 v[74:77], v[170:173], v[198:201], v[74:77]
	v_mfma_f32_16x16x32_bf16 v[70:73], v[162:165], v[206:209], v[70:73]
	v_mfma_f32_16x16x32_bf16 v[66:69], v[170:173], v[206:209], v[66:69]
	v_mfma_f32_16x16x32_bf16 v[94:97], v[166:169], v[182:185], v[94:97]
	v_mfma_f32_16x16x32_bf16 v[90:93], v[174:177], v[182:185], v[90:93]
	v_mfma_f32_16x16x32_bf16 v[86:89], v[166:169], v[194:197], v[86:89]
	v_mfma_f32_16x16x32_bf16 v[82:85], v[174:177], v[194:197], v[82:85]
	v_mfma_f32_16x16x32_bf16 v[78:81], v[166:169], v[202:205], v[78:81]
	v_mfma_f32_16x16x32_bf16 v[74:77], v[174:177], v[202:205], v[74:77]
	v_mfma_f32_16x16x32_bf16 v[70:73], v[166:169], v[210:213], v[70:73]
	v_mfma_f32_16x16x32_bf16 v[66:69], v[174:177], v[210:213], v[66:69]
	s_setprio 0
	s_barrier
	ds_read_b128 v[178:181], v135 offset:49152
	ds_read_b128 v[182:185], v135 offset:50176
	ds_read_b128 v[186:189], v135 offset:51200
	ds_read_b128 v[194:197], v135 offset:52224
	ds_read_b128 v[198:201], v135 offset:53248
	ds_read_b128 v[202:205], v135 offset:54272
	ds_read_b128 v[206:209], v135 offset:55296
	ds_read_b128 v[210:213], v135 offset:56320
	s_add_u32 s34, s33, 0x180
	s_addc_u32 s35, s63, 0
	s_mov_b32 m0, s51
	s_nop 0
	global_load_lds_dwordx4 v65, s[34:35]
	s_nop 0
	s_mov_b32 m0, s52
	s_nop 0
	global_load_lds_dwordx4 v114, s[34:35]
	s_add_u32 s34, s33, 0x40180
	s_addc_u32 s35, s63, 0
	s_mov_b32 m0, s55
	s_nop 0
	global_load_lds_dwordx4 v65, s[34:35]
	s_nop 0
	s_mov_b32 m0, s56
	s_nop 0
	global_load_lds_dwordx4 v114, s[34:35]
	s_nop 0
	s_mov_b32 m0, s53
	s_nop 0
	global_load_lds_dwordx4 v139, s[26:27]
	s_nop 0
	s_mov_b32 m0, s54
	s_nop 0
	global_load_lds_dwordx4 v138, s[26:27]
	s_waitcnt vmcnt(8)
	s_waitcnt lgkmcnt(0)
	s_barrier
	s_setprio 1
	s_waitcnt lgkmcnt(0)
	v_mfma_f32_16x16x32_bf16 v[60:63], v[146:149], v[178:181], v[60:63]
	v_mfma_f32_16x16x32_bf16 v[56:59], v[154:157], v[178:181], v[56:59]
	s_waitcnt lgkmcnt(5)
	v_mfma_f32_16x16x32_bf16 v[52:55], v[146:149], v[186:189], v[52:55]
	v_mfma_f32_16x16x32_bf16 v[48:51], v[154:157], v[186:189], v[48:51]
	s_waitcnt lgkmcnt(3)
	v_mfma_f32_16x16x32_bf16 v[44:47], v[146:149], v[198:201], v[44:47]
	v_mfma_f32_16x16x32_bf16 v[40:43], v[154:157], v[198:201], v[40:43]
	s_waitcnt lgkmcnt(1)
	v_mfma_f32_16x16x32_bf16 v[36:39], v[146:149], v[206:209], v[36:39]
	v_mfma_f32_16x16x32_bf16 v[32:35], v[154:157], v[206:209], v[32:35]
	v_mfma_f32_16x16x32_bf16 v[60:63], v[150:153], v[182:185], v[60:63]
	v_mfma_f32_16x16x32_bf16 v[56:59], v[158:161], v[182:185], v[56:59]
	v_mfma_f32_16x16x32_bf16 v[52:55], v[150:153], v[194:197], v[52:55]
	v_mfma_f32_16x16x32_bf16 v[48:51], v[158:161], v[194:197], v[48:51]
	v_mfma_f32_16x16x32_bf16 v[44:47], v[150:153], v[202:205], v[44:47]
	v_mfma_f32_16x16x32_bf16 v[40:43], v[158:161], v[202:205], v[40:43]
	s_waitcnt lgkmcnt(0)
	v_mfma_f32_16x16x32_bf16 v[36:39], v[150:153], v[210:213], v[36:39]
	v_mfma_f32_16x16x32_bf16 v[32:35], v[158:161], v[210:213], v[32:35]
	s_setprio 0
	s_setprio 1
	v_mfma_f32_16x16x32_bf16 v[28:31], v[162:165], v[178:181], v[28:31]
	v_mfma_f32_16x16x32_bf16 v[24:27], v[170:173], v[178:181], v[24:27]
	v_mfma_f32_16x16x32_bf16 v[20:23], v[162:165], v[186:189], v[20:23]
	v_mfma_f32_16x16x32_bf16 v[16:19], v[170:173], v[186:189], v[16:19]
	v_mfma_f32_16x16x32_bf16 v[12:15], v[162:165], v[198:201], v[12:15]
	v_mfma_f32_16x16x32_bf16 v[8:11], v[170:173], v[198:201], v[8:11]
	v_mfma_f32_16x16x32_bf16 v[4:7], v[162:165], v[206:209], v[4:7]
	v_mfma_f32_16x16x32_bf16 v[0:3], v[170:173], v[206:209], v[0:3]
	v_mfma_f32_16x16x32_bf16 v[28:31], v[166:169], v[182:185], v[28:31]
	v_mfma_f32_16x16x32_bf16 v[24:27], v[174:177], v[182:185], v[24:27]
	v_mfma_f32_16x16x32_bf16 v[20:23], v[166:169], v[194:197], v[20:23]
	v_mfma_f32_16x16x32_bf16 v[16:19], v[174:177], v[194:197], v[16:19]
	v_mfma_f32_16x16x32_bf16 v[12:15], v[166:169], v[202:205], v[12:15]
	v_mfma_f32_16x16x32_bf16 v[8:11], v[174:177], v[202:205], v[8:11]
	v_mfma_f32_16x16x32_bf16 v[4:7], v[166:169], v[210:213], v[4:7]
	v_mfma_f32_16x16x32_bf16 v[0:3], v[174:177], v[210:213], v[0:3]
	s_setprio 0
	s_barrier
	s_add_i32 s21, s21, 2
	s_add_u32 s2, s2, 0x100
	s_addc_u32 s3, s3, 0
	s_cmp_lt_u32 s21, 12

.LBB0_1505:
	v_mov_b32_e32 v0, 0
	s_mov_b32 s13, -2
	s_mov_b64 s[18:19], 0
	v_mov_b32_e32 v1, v0
	s_waitcnt lgkmcnt(0)
	s_add_u32 s61, s22, s18
	s_addc_u32 s66, s23, s19
	v_add_u32_e32 v132, 0x10000, v142
	v_add_u32_e32 v133, 0x14000, v142
	s_add_u32 s34, s61, 0x100
	ds_read_b128 v[134:137], v132
	ds_read_b128 v[144:147], v132 offset:1024
	ds_read_b128 v[148:151], v132 offset:2048
	ds_read_b128 v[152:155], v132 offset:3072
	ds_read_b128 v[156:159], v133
	ds_read_b128 v[160:163], v133 offset:1024
	ds_read_b128 v[164:167], v133 offset:2048
	ds_read_b128 v[168:171], v133 offset:3072
	s_addc_u32 s35, s66, 0
	s_add_u32 s26, s61, 0x180
	s_addc_u32 s27, s66, 0
	s_add_u32 s15, s24, s18
	s_addc_u32 s33, s25, s19
	s_add_u32 s62, s15, 0x100
	s_addc_u32 s63, s33, 0
	ds_read_b128 v[172:175], v143
	ds_read_b128 v[176:179], v143 offset:1024
	ds_read_b128 v[180:183], v143 offset:2048
	ds_read_b128 v[184:187], v143 offset:3072
	ds_read_b128 v[188:191], v143 offset:4096
	ds_read_b128 v[194:197], v143 offset:5120
	ds_read_b128 v[198:201], v143 offset:6144
	ds_read_b128 v[202:205], v143 offset:7168
	s_add_u32 s64, s61, 0x40080
	s_addc_u32 s65, s66, 0
	s_mov_b32 m0, s57
	s_nop 0
	global_load_lds_dwordx4 v65, s[64:65]
	s_nop 0
	s_mov_b32 m0, s58
	s_nop 0
	global_load_lds_dwordx4 v140, s[64:65]
	s_waitcnt vmcnt(8)
	s_waitcnt lgkmcnt(0)
	s_barrier
	s_setprio 1
	s_waitcnt lgkmcnt(0)
	v_mfma_f32_16x16x32_bf16 v[128:131], v[134:137], v[172:175], 0
	v_mfma_f32_16x16x32_bf16 v[124:127], v[148:151], v[172:175], 0
	s_waitcnt lgkmcnt(5)
	v_mfma_f32_16x16x32_bf16 v[120:123], v[134:137], v[180:183], 0
	v_mfma_f32_16x16x32_bf16 v[116:119], v[148:151], v[180:183], 0
	s_waitcnt lgkmcnt(3)
	v_mfma_f32_16x16x32_bf16 v[110:113], v[134:137], v[188:191], 0
	v_mfma_f32_16x16x32_bf16 v[106:109], v[148:151], v[188:191], 0
	s_waitcnt lgkmcnt(1)
	v_mfma_f32_16x16x32_bf16 v[102:105], v[134:137], v[198:201], 0
	v_mfma_f32_16x16x32_bf16 v[98:101], v[148:151], v[198:201], 0
	v_mfma_f32_16x16x32_bf16 v[128:131], v[144:147], v[176:179], v[128:131]
	v_mfma_f32_16x16x32_bf16 v[124:127], v[152:155], v[176:179], v[124:127]
	v_mfma_f32_16x16x32_bf16 v[120:123], v[144:147], v[184:187], v[120:123]
	v_mfma_f32_16x16x32_bf16 v[116:119], v[152:155], v[184:187], v[116:119]
	v_mfma_f32_16x16x32_bf16 v[110:113], v[144:147], v[194:197], v[110:113]
	v_mfma_f32_16x16x32_bf16 v[106:109], v[152:155], v[194:197], v[106:109]
	s_waitcnt lgkmcnt(0)
	v_mfma_f32_16x16x32_bf16 v[102:105], v[144:147], v[202:205], v[102:105]
	v_mfma_f32_16x16x32_bf16 v[98:101], v[152:155], v[202:205], v[98:101]
	s_setprio 0
	s_setprio 1
	v_mfma_f32_16x16x32_bf16 v[94:97], v[156:159], v[172:175], 0
	v_mfma_f32_16x16x32_bf16 v[90:93], v[164:167], v[172:175], 0
	v_mfma_f32_16x16x32_bf16 v[86:89], v[156:159], v[180:183], 0
	v_mfma_f32_16x16x32_bf16 v[82:85], v[164:167], v[180:183], 0
	v_mfma_f32_16x16x32_bf16 v[78:81], v[156:159], v[188:191], 0
	v_mfma_f32_16x16x32_bf16 v[74:77], v[164:167], v[188:191], 0
	v_mfma_f32_16x16x32_bf16 v[70:73], v[156:159], v[198:201], 0
	v_mfma_f32_16x16x32_bf16 v[66:69], v[164:167], v[198:201], 0
	v_mfma_f32_16x16x32_bf16 v[94:97], v[160:163], v[176:179], v[94:97]
	v_mfma_f32_16x16x32_bf16 v[90:93], v[168:171], v[176:179], v[90:93]
	v_mfma_f32_16x16x32_bf16 v[86:89], v[160:163], v[184:187], v[86:89]
	v_mfma_f32_16x16x32_bf16 v[82:85], v[168:171], v[184:187], v[82:85]
	v_mfma_f32_16x16x32_bf16 v[78:81], v[160:163], v[194:197], v[78:81]
	v_mfma_f32_16x16x32_bf16 v[74:77], v[168:171], v[194:197], v[74:77]
	v_mfma_f32_16x16x32_bf16 v[70:73], v[160:163], v[202:205], v[70:73]
	v_mfma_f32_16x16x32_bf16 v[66:69], v[168:171], v[202:205], v[66:69]
	s_setprio 0
	s_barrier
	ds_read_b128 v[172:175], v143 offset:16384
	ds_read_b128 v[176:179], v143 offset:17408
	ds_read_b128 v[180:183], v143 offset:18432
	ds_read_b128 v[184:187], v143 offset:19456
	ds_read_b128 v[188:191], v143 offset:20480
	ds_read_b128 v[194:197], v143 offset:21504
	ds_read_b128 v[198:201], v143 offset:22528
	ds_read_b128 v[202:205], v143 offset:23552
	s_mov_b32 m0, s41
	s_nop 0
	global_load_lds_dwordx4 v114, s[62:63]
	s_nop 0
	s_mov_b32 m0, s42
	s_nop 0
	global_load_lds_dwordx4 v141, s[62:63]
	s_add_u32 s62, s15, 0x40100
	s_addc_u32 s63, s33, 0
	s_mov_b32 m0, s43
	s_nop 0
	global_load_lds_dwordx4 v114, s[62:63]
	s_nop 0
	s_mov_b32 m0, s44
	s_nop 0
	global_load_lds_dwordx4 v141, s[62:63]
	s_mov_b32 m0, s40
	s_nop 0
	global_load_lds_dwordx4 v65, s[34:35]
	s_nop 0
	s_mov_b32 m0, s45
	s_nop 0
	global_load_lds_dwordx4 v140, s[34:35]
	s_waitcnt vmcnt(8)
	s_waitcnt lgkmcnt(0)
	s_barrier
	s_setprio 1
	s_waitcnt lgkmcnt(0)
	v_mfma_f32_16x16x32_bf16 v[60:63], v[134:137], v[172:175], 0
	v_mfma_f32_16x16x32_bf16 v[56:59], v[148:151], v[172:175], 0
	s_waitcnt lgkmcnt(5)
	v_mfma_f32_16x16x32_bf16 v[52:55], v[134:137], v[180:183], 0
	v_mfma_f32_16x16x32_bf16 v[48:51], v[148:151], v[180:183], 0
	s_waitcnt lgkmcnt(3)
	v_mfma_f32_16x16x32_bf16 v[44:47], v[134:137], v[188:191], 0
	v_mfma_f32_16x16x32_bf16 v[40:43], v[148:151], v[188:191], 0
	s_waitcnt lgkmcnt(1)
	v_mfma_f32_16x16x32_bf16 v[36:39], v[134:137], v[198:201], 0
	v_mfma_f32_16x16x32_bf16 v[32:35], v[148:151], v[198:201], 0
	v_mfma_f32_16x16x32_bf16 v[60:63], v[144:147], v[176:179], v[60:63]
	v_mfma_f32_16x16x32_bf16 v[56:59], v[152:155], v[176:179], v[56:59]
	v_mfma_f32_16x16x32_bf16 v[52:55], v[144:147], v[184:187], v[52:55]
	v_mfma_f32_16x16x32_bf16 v[48:51], v[152:155], v[184:187], v[48:51]
	v_mfma_f32_16x16x32_bf16 v[44:47], v[144:147], v[194:197], v[44:47]
	v_mfma_f32_16x16x32_bf16 v[40:43], v[152:155], v[194:197], v[40:43]
	s_waitcnt lgkmcnt(0)
	v_mfma_f32_16x16x32_bf16 v[36:39], v[144:147], v[202:205], v[36:39]
	v_mfma_f32_16x16x32_bf16 v[32:35], v[152:155], v[202:205], v[32:35]
	s_setprio 0
	s_setprio 1
	v_mfma_f32_16x16x32_bf16 v[28:31], v[156:159], v[172:175], 0
	v_mfma_f32_16x16x32_bf16 v[24:27], v[164:167], v[172:175], 0
	v_mfma_f32_16x16x32_bf16 v[20:23], v[156:159], v[180:183], 0
	v_mfma_f32_16x16x32_bf16 v[16:19], v[164:167], v[180:183], 0
	v_mfma_f32_16x16x32_bf16 v[12:15], v[156:159], v[188:191], 0
	v_mfma_f32_16x16x32_bf16 v[8:11], v[164:167], v[188:191], 0
	v_mfma_f32_16x16x32_bf16 v[4:7], v[156:159], v[198:201], 0
	v_mfma_f32_16x16x32_bf16 v[0:3], v[164:167], v[198:201], 0
	v_mfma_f32_16x16x32_bf16 v[28:31], v[160:163], v[176:179], v[28:31]
	v_mfma_f32_16x16x32_bf16 v[24:27], v[168:171], v[176:179], v[24:27]
	v_mfma_f32_16x16x32_bf16 v[20:23], v[160:163], v[184:187], v[20:23]
	v_mfma_f32_16x16x32_bf16 v[16:19], v[168:171], v[184:187], v[16:19]
	v_mfma_f32_16x16x32_bf16 v[12:15], v[160:163], v[194:197], v[12:15]
	v_mfma_f32_16x16x32_bf16 v[8:11], v[168:171], v[194:197], v[8:11]
	v_mfma_f32_16x16x32_bf16 v[4:7], v[160:163], v[202:205], v[4:7]
	v_mfma_f32_16x16x32_bf16 v[0:3], v[168:171], v[202:205], v[0:3]
	s_setprio 0
	s_barrier
	v_add_u32_e32 v134, 0x18000, v142
	v_add_u32_e32 v135, 0x1c000, v142
	ds_read_b128 v[136:139], v134
	ds_read_b128 v[144:147], v134 offset:1024
	ds_read_b128 v[148:151], v134 offset:2048
	ds_read_b128 v[152:155], v134 offset:3072
	ds_read_b128 v[156:159], v135
	ds_read_b128 v[160:163], v135 offset:1024
	ds_read_b128 v[164:167], v135 offset:2048
	ds_read_b128 v[168:171], v135 offset:3072
	ds_read_b128 v[172:175], v143 offset:32768
	ds_read_b128 v[176:179], v143 offset:33792
	ds_read_b128 v[180:183], v143 offset:34816
	ds_read_b128 v[184:187], v143 offset:35840
	ds_read_b128 v[188:191], v143 offset:36864
	ds_read_b128 v[194:197], v143 offset:37888
	ds_read_b128 v[198:201], v143 offset:38912
	ds_read_b128 v[202:205], v143 offset:39936
	s_add_u32 s34, s61, 0x40100
	s_addc_u32 s35, s66, 0
	s_mov_b32 m0, s46
	s_nop 0
	global_load_lds_dwordx4 v65, s[34:35]
	s_nop 0
	s_mov_b32 m0, s47
	s_nop 0
	global_load_lds_dwordx4 v140, s[34:35]
	s_waitcnt vmcnt(8)
	s_waitcnt lgkmcnt(0)
	s_barrier
	s_setprio 1
	s_waitcnt lgkmcnt(0)
	v_mfma_f32_16x16x32_bf16 v[128:131], v[136:139], v[172:175], v[128:131]
	v_mfma_f32_16x16x32_bf16 v[124:127], v[148:151], v[172:175], v[124:127]
	s_waitcnt lgkmcnt(5)
	v_mfma_f32_16x16x32_bf16 v[120:123], v[136:139], v[180:183], v[120:123]
	v_mfma_f32_16x16x32_bf16 v[116:119], v[148:151], v[180:183], v[116:119]
	s_waitcnt lgkmcnt(3)
	v_mfma_f32_16x16x32_bf16 v[110:113], v[136:139], v[188:191], v[110:113]
	v_mfma_f32_16x16x32_bf16 v[106:109], v[148:151], v[188:191], v[106:109]
	s_waitcnt lgkmcnt(1)
	v_mfma_f32_16x16x32_bf16 v[102:105], v[136:139], v[198:201], v[102:105]
	v_mfma_f32_16x16x32_bf16 v[98:101], v[148:151], v[198:201], v[98:101]
	v_mfma_f32_16x16x32_bf16 v[128:131], v[144:147], v[176:179], v[128:131]
	v_mfma_f32_16x16x32_bf16 v[124:127], v[152:155], v[176:179], v[124:127]
	v_mfma_f32_16x16x32_bf16 v[120:123], v[144:147], v[184:187], v[120:123]
	v_mfma_f32_16x16x32_bf16 v[116:119], v[152:155], v[184:187], v[116:119]
	v_mfma_f32_16x16x32_bf16 v[110:113], v[144:147], v[194:197], v[110:113]
	v_mfma_f32_16x16x32_bf16 v[106:109], v[152:155], v[194:197], v[106:109]
	s_waitcnt lgkmcnt(0)
	v_mfma_f32_16x16x32_bf16 v[102:105], v[144:147], v[202:205], v[102:105]
	v_mfma_f32_16x16x32_bf16 v[98:101], v[152:155], v[202:205], v[98:101]
	s_setprio 0
	s_setprio 1
	v_mfma_f32_16x16x32_bf16 v[94:97], v[156:159], v[172:175], v[94:97]
	v_mfma_f32_16x16x32_bf16 v[90:93], v[164:167], v[172:175], v[90:93]
	v_mfma_f32_16x16x32_bf16 v[86:89], v[156:159], v[180:183], v[86:89]
	v_mfma_f32_16x16x32_bf16 v[82:85], v[164:167], v[180:183], v[82:85]
	v_mfma_f32_16x16x32_bf16 v[78:81], v[156:159], v[188:191], v[78:81]
	v_mfma_f32_16x16x32_bf16 v[74:77], v[164:167], v[188:191], v[74:77]
	v_mfma_f32_16x16x32_bf16 v[70:73], v[156:159], v[198:201], v[70:73]
	v_mfma_f32_16x16x32_bf16 v[66:69], v[164:167], v[198:201], v[66:69]
	v_mfma_f32_16x16x32_bf16 v[94:97], v[160:163], v[176:179], v[94:97]
	v_mfma_f32_16x16x32_bf16 v[90:93], v[168:171], v[176:179], v[90:93]
	v_mfma_f32_16x16x32_bf16 v[86:89], v[160:163], v[184:187], v[86:89]
	v_mfma_f32_16x16x32_bf16 v[82:85], v[168:171], v[184:187], v[82:85]
	v_mfma_f32_16x16x32_bf16 v[78:81], v[160:163], v[194:197], v[78:81]
	v_mfma_f32_16x16x32_bf16 v[74:77], v[168:171], v[194:197], v[74:77]
	v_mfma_f32_16x16x32_bf16 v[70:73], v[160:163], v[202:205], v[70:73]
	v_mfma_f32_16x16x32_bf16 v[66:69], v[168:171], v[202:205], v[66:69]
	s_setprio 0
	s_barrier
	ds_read_b128 v[172:175], v143 offset:49152
	ds_read_b128 v[176:179], v143 offset:50176
	ds_read_b128 v[180:183], v143 offset:51200
	ds_read_b128 v[184:187], v143 offset:52224
	ds_read_b128 v[188:191], v143 offset:53248
	ds_read_b128 v[194:197], v143 offset:54272
	ds_read_b128 v[198:201], v143 offset:55296
	ds_read_b128 v[202:205], v143 offset:56320
	s_add_u32 s34, s15, 0x180
	s_addc_u32 s35, s33, 0
	s_mov_b32 m0, s51
	s_nop 0
	global_load_lds_dwordx4 v114, s[34:35]
	s_nop 0
	s_mov_b32 m0, s52
	s_nop 0
	global_load_lds_dwordx4 v141, s[34:35]
	s_add_u32 s34, s15, 0x40180
	s_addc_u32 s35, s33, 0
	s_mov_b32 m0, s55
	s_nop 0
	global_load_lds_dwordx4 v114, s[34:35]
	s_nop 0
	s_mov_b32 m0, s56
	s_nop 0
	global_load_lds_dwordx4 v141, s[34:35]
	s_nop 0
	s_mov_b32 m0, s53
	s_nop 0
	global_load_lds_dwordx4 v65, s[26:27]
	s_nop 0
	s_mov_b32 m0, s54
	s_nop 0
	global_load_lds_dwordx4 v140, s[26:27]
	s_waitcnt vmcnt(8)
	s_waitcnt lgkmcnt(0)
	s_barrier
	s_setprio 1
	s_waitcnt lgkmcnt(0)
	v_mfma_f32_16x16x32_bf16 v[60:63], v[136:139], v[172:175], v[60:63]
	v_mfma_f32_16x16x32_bf16 v[56:59], v[148:151], v[172:175], v[56:59]
	s_waitcnt lgkmcnt(5)
	v_mfma_f32_16x16x32_bf16 v[52:55], v[136:139], v[180:183], v[52:55]
	v_mfma_f32_16x16x32_bf16 v[48:51], v[148:151], v[180:183], v[48:51]
	s_waitcnt lgkmcnt(3)
	v_mfma_f32_16x16x32_bf16 v[44:47], v[136:139], v[188:191], v[44:47]
	v_mfma_f32_16x16x32_bf16 v[40:43], v[148:151], v[188:191], v[40:43]
	s_waitcnt lgkmcnt(1)
	v_mfma_f32_16x16x32_bf16 v[36:39], v[136:139], v[198:201], v[36:39]
	v_mfma_f32_16x16x32_bf16 v[32:35], v[148:151], v[198:201], v[32:35]
	v_mfma_f32_16x16x32_bf16 v[60:63], v[144:147], v[176:179], v[60:63]
	v_mfma_f32_16x16x32_bf16 v[56:59], v[152:155], v[176:179], v[56:59]
	v_mfma_f32_16x16x32_bf16 v[52:55], v[144:147], v[184:187], v[52:55]
	v_mfma_f32_16x16x32_bf16 v[48:51], v[152:155], v[184:187], v[48:51]
	v_mfma_f32_16x16x32_bf16 v[44:47], v[144:147], v[194:197], v[44:47]
	v_mfma_f32_16x16x32_bf16 v[40:43], v[152:155], v[194:197], v[40:43]
	s_waitcnt lgkmcnt(0)
	v_mfma_f32_16x16x32_bf16 v[36:39], v[144:147], v[202:205], v[36:39]
	v_mfma_f32_16x16x32_bf16 v[32:35], v[152:155], v[202:205], v[32:35]
	s_setprio 0
	s_setprio 1
	v_mfma_f32_16x16x32_bf16 v[28:31], v[156:159], v[172:175], v[28:31]
	v_mfma_f32_16x16x32_bf16 v[24:27], v[164:167], v[172:175], v[24:27]
	v_mfma_f32_16x16x32_bf16 v[20:23], v[156:159], v[180:183], v[20:23]
	v_mfma_f32_16x16x32_bf16 v[16:19], v[164:167], v[180:183], v[16:19]
	v_mfma_f32_16x16x32_bf16 v[12:15], v[156:159], v[188:191], v[12:15]
	v_mfma_f32_16x16x32_bf16 v[8:11], v[164:167], v[188:191], v[8:11]
	v_mfma_f32_16x16x32_bf16 v[4:7], v[156:159], v[198:201], v[4:7]
	v_mfma_f32_16x16x32_bf16 v[0:3], v[164:167], v[198:201], v[0:3]
	v_mfma_f32_16x16x32_bf16 v[28:31], v[160:163], v[176:179], v[28:31]
	v_mfma_f32_16x16x32_bf16 v[24:27], v[168:171], v[176:179], v[24:27]
	v_mfma_f32_16x16x32_bf16 v[20:23], v[160:163], v[184:187], v[20:23]
	v_mfma_f32_16x16x32_bf16 v[16:19], v[168:171], v[184:187], v[16:19]
	v_mfma_f32_16x16x32_bf16 v[12:15], v[160:163], v[194:197], v[12:15]
	v_mfma_f32_16x16x32_bf16 v[8:11], v[168:171], v[194:197], v[8:11]
	v_mfma_f32_16x16x32_bf16 v[4:7], v[160:163], v[202:205], v[4:7]
	v_mfma_f32_16x16x32_bf16 v[0:3], v[168:171], v[202:205], v[0:3]
	s_setprio 0
	s_barrier
	s_add_i32 s13, s13, 2
	s_add_u32 s18, s18, 0x100
	s_addc_u32 s19, s19, 0
	s_cmp_lt_u32 s13, 12
